# final phase software-pipelined: the four row pairs of a wave unrolled, the expert-row loads of the next pair (second register bank, fixed 16 loads per pair) issued before the current pair is waited fo
# baseline (speedup 1.0000x reference)
.LBB0_1241:
	s_or_b64 exec, exec, s[0:1]
	s_waitcnt lgkmcnt(0)
	s_barrier
	v_readlane_b32 s6, v235, 16
	v_and_b32_e32 v0, 63, v186
	v_lshrrev_b32_e32 v11, 6, v186
	s_load_dwordx2 s[4:5], s[46:47], 0x98
	s_load_dwordx4 s[0:3], s[46:47], 0x88
	v_readfirstlane_b32 s8, v11
	v_lshlrev_b32_e32 v1, 4, v0
	v_lshlrev_b32_e32 v11, 14, v11
	v_add_u32_e32 v11, v11, v1
	v_lshlrev_b32_e32 v2, 5, v0
	v_and_b32_e32 v3, 31, v0
	v_lshlrev_b32_e32 v3, 2, v3
	v_xor_b32_e32 v4, 32, v0
	v_lshlrev_b32_e32 v4, 2, v4
	v_xor_b32_e32 v5, 16, v0
	v_lshlrev_b32_e32 v5, 2, v5
	v_xor_b32_e32 v6, 8, v0
	v_lshlrev_b32_e32 v6, 2, v6
	v_xor_b32_e32 v7, 4, v0
	v_lshlrev_b32_e32 v7, 2, v7
	v_xor_b32_e32 v8, 2, v0
	v_lshlrev_b32_e32 v8, 2, v8
	v_xor_b32_e32 v9, 1, v0
	v_lshlrev_b32_e32 v9, 2, v9
	v_mov_b32_e32 v10, 0x358637bd
	s_lshl_b32 s6, s6, 4
	s_lshl_b32 s8, s8, 1
	s_add_i32 s6, s6, s8
	s_mov_b32 s23, 0x3a800000
	s_waitcnt lgkmcnt(0)
	s_add_u32 s14, s4, 0x1b73000
	s_addc_u32 s15, s5, 0
	s_add_u32 s18, s4, 0x15b000
	s_addc_u32 s19, s5, 0
	s_add_u32 s20, s4, 0x5000
	s_addc_u32 s21, s5, 0
	s_add_u32 s34, s20, 0x6000
	s_addc_u32 s35, s21, 0
	global_load_dwordx4 v[12:15], v2, s[0:1]
	global_load_dwordx4 v[16:19], v2, s[0:1] offset:16
	global_load_dwordx4 v[20:23], v2, s[0:1] offset:2048
	global_load_dwordx4 v[24:27], v2, s[0:1] offset:2064
	global_load_dwordx4 v[28:31], v2, s[20:21]
	global_load_dwordx4 v[32:35], v2, s[20:21] offset:16
	global_load_dwordx4 v[36:39], v2, s[20:21] offset:2048
	global_load_dwordx4 v[40:43], v2, s[20:21] offset:2064
	s_add_i32 s8, s6, 0
	s_lshl_b32 s26, s8, 6
	s_add_u32 s24, s18, s26
	s_addc_u32 s25, s19, 0
	global_load_dword v44, v3, s[24:25]
	s_add_i32 s8, s6, 4096
	s_lshl_b32 s26, s8, 6
	s_add_u32 s24, s18, s26
	s_addc_u32 s25, s19, 0
	global_load_dword v45, v3, s[24:25]
	s_add_i32 s8, s6, 8192
	s_lshl_b32 s26, s8, 6
	s_add_u32 s24, s18, s26
	s_addc_u32 s25, s19, 0
	global_load_dword v46, v3, s[24:25]
	s_add_i32 s8, s6, 12288
	s_lshl_b32 s26, s8, 6
	s_add_u32 s24, s18, s26
	s_addc_u32 s25, s19, 0
	global_load_dword v47, v3, s[24:25]
	s_waitcnt vmcnt(0)
	v_readfirstlane_b32 s100, v186
	s_nop 0
	s_cmp_lg_u32 s100, 0
	s_cbranch_scc1 .Lp11_w_skip
	s_cmp_eq_u32 s98, 0
	s_cbranch_scc1 .Lp11_w_skip
	v_readlane_b32 s100, v235, 7
	v_readlane_b32 s101, v235, 8
	v_mov_b32_e32 v236, 0x3400
	v_mov_b32_e32 v239, 0
	s_nop 3

.Lp11_w_skip:
	s_barrier
	v_cmp_lt_i32_e32 vcc, -1, v44
	s_mov_b32 s22, 0
	s_and_b32 s9, vcc_lo, 0xffff
	s_lshr_b32 s10, vcc_lo, 16
	s_and_b32 s10, s10, 0xffff
	s_cmp_eq_u32 s9, 0
	s_cbranch_scc1 .Lfin_dm0_0_0
	s_ff1_i32_b32 s26, s9
	s_bitset0_b32 s9, s26
	v_readlane_b32 s30, v44, s26
	s_lshl_b32 s26, s26, 11
	s_add_i32 s26, s26, s22
	s_add_i32 s26, s26, s30
	s_lshl_b32 s26, s26, 11
	s_add_u32 s24, s14, s26
	s_addc_u32 s25, s15, 0
	s_branch .Lfin_go0_0_0
.Lfin_dm0_0_0:
	s_mov_b32 s24, s14
	s_mov_b32 s25, s15
.Lfin_go0_0_0:
	global_load_dwordx4 v[128:131], v1, s[24:25]
	global_load_dwordx4 v[132:135], v1, s[24:25] offset:1024
	s_cmp_eq_u32 s9, 0
	s_cbranch_scc1 .Lfin_dm0_0_1
	s_ff1_i32_b32 s26, s9
	s_bitset0_b32 s9, s26
	v_readlane_b32 s30, v44, s26
	s_lshl_b32 s26, s26, 11
	s_add_i32 s26, s26, s22
	s_add_i32 s26, s26, s30
	s_lshl_b32 s26, s26, 11
	s_add_u32 s24, s14, s26
	s_addc_u32 s25, s15, 0
	s_branch .Lfin_go0_0_1

.Lfin_go0_0_1:
	global_load_dwordx4 v[136:139], v1, s[24:25]
	global_load_dwordx4 v[140:143], v1, s[24:25] offset:1024
	s_cmp_eq_u32 s9, 0
	s_cbranch_scc1 .Lfin_dm0_0_2
	s_ff1_i32_b32 s26, s9
	s_bitset0_b32 s9, s26
	v_readlane_b32 s30, v44, s26
	s_lshl_b32 s26, s26, 11
	s_add_i32 s26, s26, s22
	s_add_i32 s26, s26, s30
	s_lshl_b32 s26, s26, 11
	s_add_u32 s24, s14, s26
	s_addc_u32 s25, s15, 0
	s_branch .Lfin_go0_0_2

.Lfin_go0_0_2:
	global_load_dwordx4 v[144:147], v1, s[24:25]
	global_load_dwordx4 v[148:151], v1, s[24:25] offset:1024
	s_cmp_eq_u32 s9, 0
	s_cbranch_scc1 .Lfin_dm0_0_3
	s_ff1_i32_b32 s26, s9
	s_bitset0_b32 s9, s26
	v_readlane_b32 s30, v44, s26
	s_lshl_b32 s26, s26, 11
	s_add_i32 s26, s26, s22
	s_add_i32 s26, s26, s30
	s_lshl_b32 s26, s26, 11
	s_add_u32 s24, s14, s26
	s_addc_u32 s25, s15, 0
	s_branch .Lfin_go0_0_3

.Lfin_go0_0_3:
	global_load_dwordx4 v[152:155], v1, s[24:25]
	global_load_dwordx4 v[156:159], v1, s[24:25] offset:1024
	s_cmp_eq_u32 s10, 0
	s_cbranch_scc1 .Lfin_dm0_1_0
	s_ff1_i32_b32 s26, s10
	s_bitset0_b32 s10, s26
	s_add_i32 s27, s26, 16
	v_readlane_b32 s30, v44, s27
	s_lshl_b32 s26, s26, 11
	s_add_i32 s26, s26, s22
	s_add_i32 s26, s26, s30
	s_lshl_b32 s26, s26, 11
	s_add_u32 s24, s14, s26
	s_addc_u32 s25, s15, 0
	s_branch .Lfin_go0_1_0

.Lfin_go0_1_0:
	global_load_dwordx4 v[160:163], v1, s[24:25]
	global_load_dwordx4 v[164:167], v1, s[24:25] offset:1024
	s_cmp_eq_u32 s10, 0
	s_cbranch_scc1 .Lfin_dm0_1_1
	s_ff1_i32_b32 s26, s10
	s_bitset0_b32 s10, s26
	s_add_i32 s27, s26, 16
	v_readlane_b32 s30, v44, s27
	s_lshl_b32 s26, s26, 11
	s_add_i32 s26, s26, s22
	s_add_i32 s26, s26, s30
	s_lshl_b32 s26, s26, 11
	s_add_u32 s24, s14, s26
	s_addc_u32 s25, s15, 0
	s_branch .Lfin_go0_1_1

.Lfin_go0_1_1:
	global_load_dwordx4 v[168:171], v1, s[24:25]
	global_load_dwordx4 v[172:175], v1, s[24:25] offset:1024
	s_cmp_eq_u32 s10, 0
	s_cbranch_scc1 .Lfin_dm0_1_2
	s_ff1_i32_b32 s26, s10
	s_bitset0_b32 s10, s26
	s_add_i32 s27, s26, 16
	v_readlane_b32 s30, v44, s27
	s_lshl_b32 s26, s26, 11
	s_add_i32 s26, s26, s22
	s_add_i32 s26, s26, s30
	s_lshl_b32 s26, s26, 11
	s_add_u32 s24, s14, s26
	s_addc_u32 s25, s15, 0
	s_branch .Lfin_go0_1_2

.Lfin_go0_1_2:
	global_load_dwordx4 v[176:179], v1, s[24:25]
	global_load_dwordx4 v[180:183], v1, s[24:25] offset:1024
	s_cmp_eq_u32 s10, 0
	s_cbranch_scc1 .Lfin_dm0_1_3
	s_ff1_i32_b32 s26, s10
	s_bitset0_b32 s10, s26
	s_add_i32 s27, s26, 16
	v_readlane_b32 s30, v44, s27
	s_lshl_b32 s26, s26, 11
	s_add_i32 s26, s26, s22
	s_add_i32 s26, s26, s30
	s_lshl_b32 s26, s26, 11
	s_add_u32 s24, s14, s26
	s_addc_u32 s25, s15, 0
	s_branch .Lfin_go0_1_3

.Lfin_go0_1_3:
	global_load_dwordx4 v[184:187], v1, s[24:25]
	global_load_dwordx4 v[188:191], v1, s[24:25] offset:1024
	v_cmp_lt_i32_e32 vcc, -1, v45
	s_mov_b32 s22, 0
	s_and_b32 s9, vcc_lo, 0xffff
	s_lshr_b32 s10, vcc_lo, 16
	s_and_b32 s10, s10, 0xffff
	s_cmp_eq_u32 s9, 0
	s_cbranch_scc1 .Lfin_dm1_0_0
	s_ff1_i32_b32 s26, s9
	s_bitset0_b32 s9, s26
	v_readlane_b32 s30, v45, s26
	s_lshl_b32 s26, s26, 11
	s_add_i32 s26, s26, s22
	s_add_i32 s26, s26, s30
	s_lshl_b32 s26, s26, 11
	s_add_u32 s24, s14, s26
	s_addc_u32 s25, s15, 0
	s_branch .Lfin_go1_0_0

.Lfin_go1_0_0:
	global_load_dwordx4 v[192:195], v1, s[24:25]
	global_load_dwordx4 v[196:199], v1, s[24:25] offset:1024
	s_cmp_eq_u32 s9, 0
	s_cbranch_scc1 .Lfin_dm1_0_1
	s_ff1_i32_b32 s26, s9
	s_bitset0_b32 s9, s26
	v_readlane_b32 s30, v45, s26
	s_lshl_b32 s26, s26, 11
	s_add_i32 s26, s26, s22
	s_add_i32 s26, s26, s30
	s_lshl_b32 s26, s26, 11
	s_add_u32 s24, s14, s26
	s_addc_u32 s25, s15, 0
	s_branch .Lfin_go1_0_1

.Lfin_go1_0_1:
	global_load_dwordx4 v[200:203], v1, s[24:25]
	global_load_dwordx4 v[204:207], v1, s[24:25] offset:1024
	s_cmp_eq_u32 s9, 0
	s_cbranch_scc1 .Lfin_dm1_0_2
	s_ff1_i32_b32 s26, s9
	s_bitset0_b32 s9, s26
	v_readlane_b32 s30, v45, s26
	s_lshl_b32 s26, s26, 11
	s_add_i32 s26, s26, s22
	s_add_i32 s26, s26, s30
	s_lshl_b32 s26, s26, 11
	s_add_u32 s24, s14, s26
	s_addc_u32 s25, s15, 0
	s_branch .Lfin_go1_0_2

.Lfin_go1_0_2:
	global_load_dwordx4 v[208:211], v1, s[24:25]
	global_load_dwordx4 v[212:215], v1, s[24:25] offset:1024
	s_cmp_eq_u32 s9, 0
	s_cbranch_scc1 .Lfin_dm1_0_3
	s_ff1_i32_b32 s26, s9
	s_bitset0_b32 s9, s26
	v_readlane_b32 s30, v45, s26
	s_lshl_b32 s26, s26, 11
	s_add_i32 s26, s26, s22
	s_add_i32 s26, s26, s30
	s_lshl_b32 s26, s26, 11
	s_add_u32 s24, s14, s26
	s_addc_u32 s25, s15, 0
	s_branch .Lfin_go1_0_3

.Lfin_go1_0_3:
	global_load_dwordx4 v[216:219], v1, s[24:25]
	global_load_dwordx4 v[220:223], v1, s[24:25] offset:1024
	s_cmp_eq_u32 s10, 0
	s_cbranch_scc1 .Lfin_dm1_1_0
	s_ff1_i32_b32 s26, s10
	s_bitset0_b32 s10, s26
	s_add_i32 s27, s26, 16
	v_readlane_b32 s30, v45, s27
	s_lshl_b32 s26, s26, 11
	s_add_i32 s26, s26, s22
	s_add_i32 s26, s26, s30
	s_lshl_b32 s26, s26, 11
	s_add_u32 s24, s14, s26
	s_addc_u32 s25, s15, 0
	s_branch .Lfin_go1_1_0

.Lfin_go1_1_0:
	global_load_dwordx4 v[224:227], v1, s[24:25]
	global_load_dwordx4 v[228:231], v1, s[24:25] offset:1024
	s_cmp_eq_u32 s10, 0
	s_cbranch_scc1 .Lfin_dm1_1_1
	s_ff1_i32_b32 s26, s10
	s_bitset0_b32 s10, s26
	s_add_i32 s27, s26, 16
	v_readlane_b32 s30, v45, s27
	s_lshl_b32 s26, s26, 11
	s_add_i32 s26, s26, s22
	s_add_i32 s26, s26, s30
	s_lshl_b32 s26, s26, 11
	s_add_u32 s24, s14, s26
	s_addc_u32 s25, s15, 0
	s_branch .Lfin_go1_1_1

.Lfin_go1_1_1:
	global_load_dwordx4 v[232:235], v1, s[24:25]
	global_load_dwordx4 v[236:239], v1, s[24:25] offset:1024
	s_cmp_eq_u32 s10, 0
	s_cbranch_scc1 .Lfin_dm1_1_2
	s_ff1_i32_b32 s26, s10
	s_bitset0_b32 s10, s26
	s_add_i32 s27, s26, 16
	v_readlane_b32 s30, v45, s27
	s_lshl_b32 s26, s26, 11
	s_add_i32 s26, s26, s22
	s_add_i32 s26, s26, s30
	s_lshl_b32 s26, s26, 11
	s_add_u32 s24, s14, s26
	s_addc_u32 s25, s15, 0
	s_branch .Lfin_go1_1_2

.Lfin_go1_1_2:
	global_load_dwordx4 v[240:243], v1, s[24:25]
	global_load_dwordx4 v[244:247], v1, s[24:25] offset:1024
	s_cmp_eq_u32 s10, 0
	s_cbranch_scc1 .Lfin_dm1_1_3
	s_ff1_i32_b32 s26, s10
	s_bitset0_b32 s10, s26
	s_add_i32 s27, s26, 16
	v_readlane_b32 s30, v45, s27
	s_lshl_b32 s26, s26, 11
	s_add_i32 s26, s26, s22
	s_add_i32 s26, s26, s30
	s_lshl_b32 s26, s26, 11
	s_add_u32 s24, s14, s26
	s_addc_u32 s25, s15, 0
	s_branch .Lfin_go1_1_3

.Lfin_go1_1_3:
	global_load_dwordx4 v[248:251], v1, s[24:25]
	global_load_dwordx4 v[252:255], v1, s[24:25] offset:1024
	s_waitcnt vmcnt(16)
	ds_read_b128 v[88:91], v11
	ds_read_b128 v[92:95], v11 offset:1024
	ds_read_b128 v[96:99], v11 offset:2048
	ds_read_b128 v[100:103], v11 offset:3072
	v_add_u32_e32 v11, 0x1000, v11
	s_waitcnt lgkmcnt(0)
	v_cvt_f32_f16_e32 v56, v88
	v_cvt_f32_f16_sdwa v57, v88 dst_sel:DWORD dst_unused:UNUSED_PAD src0_sel:WORD_1
	v_cvt_f32_f16_e32 v58, v89
	v_cvt_f32_f16_sdwa v59, v89 dst_sel:DWORD dst_unused:UNUSED_PAD src0_sel:WORD_1
	v_cvt_f32_f16_e32 v60, v90
	v_cvt_f32_f16_sdwa v61, v90 dst_sel:DWORD dst_unused:UNUSED_PAD src0_sel:WORD_1
	v_cvt_f32_f16_e32 v62, v91
	v_cvt_f32_f16_sdwa v63, v91 dst_sel:DWORD dst_unused:UNUSED_PAD src0_sel:WORD_1
	v_cvt_f32_f16_e32 v64, v92
	v_cvt_f32_f16_sdwa v65, v92 dst_sel:DWORD dst_unused:UNUSED_PAD src0_sel:WORD_1
	v_cvt_f32_f16_e32 v66, v93
	v_cvt_f32_f16_sdwa v67, v93 dst_sel:DWORD dst_unused:UNUSED_PAD src0_sel:WORD_1
	v_cvt_f32_f16_e32 v68, v94
	v_cvt_f32_f16_sdwa v69, v94 dst_sel:DWORD dst_unused:UNUSED_PAD src0_sel:WORD_1
	v_cvt_f32_f16_e32 v70, v95
	v_cvt_f32_f16_sdwa v71, v95 dst_sel:DWORD dst_unused:UNUSED_PAD src0_sel:WORD_1
	v_cvt_f32_f16_e32 v72, v96
	v_cvt_f32_f16_sdwa v73, v96 dst_sel:DWORD dst_unused:UNUSED_PAD src0_sel:WORD_1
	v_cvt_f32_f16_e32 v74, v97
	v_cvt_f32_f16_sdwa v75, v97 dst_sel:DWORD dst_unused:UNUSED_PAD src0_sel:WORD_1
	v_cvt_f32_f16_e32 v76, v98
	v_cvt_f32_f16_sdwa v77, v98 dst_sel:DWORD dst_unused:UNUSED_PAD src0_sel:WORD_1
	v_cvt_f32_f16_e32 v78, v99
	v_cvt_f32_f16_sdwa v79, v99 dst_sel:DWORD dst_unused:UNUSED_PAD src0_sel:WORD_1
	v_cvt_f32_f16_e32 v80, v100
	v_cvt_f32_f16_sdwa v81, v100 dst_sel:DWORD dst_unused:UNUSED_PAD src0_sel:WORD_1
	v_cvt_f32_f16_e32 v82, v101
	v_cvt_f32_f16_sdwa v83, v101 dst_sel:DWORD dst_unused:UNUSED_PAD src0_sel:WORD_1
	v_cvt_f32_f16_e32 v84, v102
	v_cvt_f32_f16_sdwa v85, v102 dst_sel:DWORD dst_unused:UNUSED_PAD src0_sel:WORD_1
	v_cvt_f32_f16_e32 v86, v103
	v_cvt_f32_f16_sdwa v87, v103 dst_sel:DWORD dst_unused:UNUSED_PAD src0_sel:WORD_1
	v_cmp_lt_i32_e32 vcc, -1, v44
	s_mov_b32 s22, 0
	s_and_b32 s9, vcc_lo, 0xffff
	s_lshr_b32 s10, vcc_lo, 16
	s_and_b32 s10, s10, 0xffff
	s_bcnt1_i32_b32 s11, s9
	s_bcnt1_i32_b32 s12, s10
	v_mov_b32_e32 v88, 0
	v_mov_b32_e32 v89, 0
	v_mov_b32_e32 v90, 0
	v_mov_b32_e32 v91, 0
	v_mov_b32_e32 v92, 0
	v_mov_b32_e32 v93, 0
	v_mov_b32_e32 v94, 0
	v_mov_b32_e32 v95, 0
	v_mov_b32_e32 v96, 0
	v_mov_b32_e32 v97, 0
	v_mov_b32_e32 v98, 0
	v_mov_b32_e32 v99, 0
	v_mov_b32_e32 v100, 0
	v_mov_b32_e32 v101, 0
	v_mov_b32_e32 v102, 0
	v_mov_b32_e32 v103, 0
	v_mov_b32_e32 v104, 0
	v_mov_b32_e32 v105, 0
	v_mov_b32_e32 v106, 0
	v_mov_b32_e32 v107, 0
	v_mov_b32_e32 v108, 0
	v_mov_b32_e32 v109, 0
	v_mov_b32_e32 v110, 0
	v_mov_b32_e32 v111, 0
	v_mov_b32_e32 v112, 0
	v_mov_b32_e32 v113, 0
	v_mov_b32_e32 v114, 0
	v_mov_b32_e32 v115, 0
	v_mov_b32_e32 v116, 0
	v_mov_b32_e32 v117, 0
	v_mov_b32_e32 v118, 0
	v_mov_b32_e32 v119, 0
	s_add_i32 s26, s9, -1
	s_and_b32 s9, s9, s26
	s_add_i32 s26, s9, -1
	s_and_b32 s9, s9, s26
	s_add_i32 s26, s9, -1
	s_and_b32 s9, s9, s26
	s_add_i32 s26, s9, -1
	s_and_b32 s9, s9, s26
	s_cmp_lt_u32 s11, 1
	s_cbranch_scc1 .Lfin_accd0_0
	v_lshlrev_b32_e32 v48, 16, v128
	v_and_b32_e32 v49, 0xffff0000, v128
	v_pk_add_f32 v[88:89], v[88:89], v[48:49]
	v_lshlrev_b32_e32 v48, 16, v129
	v_and_b32_e32 v49, 0xffff0000, v129
	v_pk_add_f32 v[90:91], v[90:91], v[48:49]
	v_lshlrev_b32_e32 v48, 16, v130
	v_and_b32_e32 v49, 0xffff0000, v130
	v_pk_add_f32 v[92:93], v[92:93], v[48:49]
	v_lshlrev_b32_e32 v48, 16, v131
	v_and_b32_e32 v49, 0xffff0000, v131
	v_pk_add_f32 v[94:95], v[94:95], v[48:49]
	v_lshlrev_b32_e32 v48, 16, v132
	v_and_b32_e32 v49, 0xffff0000, v132
	v_pk_add_f32 v[96:97], v[96:97], v[48:49]
	v_lshlrev_b32_e32 v48, 16, v133
	v_and_b32_e32 v49, 0xffff0000, v133
	v_pk_add_f32 v[98:99], v[98:99], v[48:49]
	v_lshlrev_b32_e32 v48, 16, v134
	v_and_b32_e32 v49, 0xffff0000, v134
	v_pk_add_f32 v[100:101], v[100:101], v[48:49]
	v_lshlrev_b32_e32 v48, 16, v135
	v_and_b32_e32 v49, 0xffff0000, v135
	v_pk_add_f32 v[102:103], v[102:103], v[48:49]
	s_cmp_lt_u32 s11, 2
	s_cbranch_scc1 .Lfin_accd0_0
	v_lshlrev_b32_e32 v48, 16, v136
	v_and_b32_e32 v49, 0xffff0000, v136
	v_pk_add_f32 v[88:89], v[88:89], v[48:49]
	v_lshlrev_b32_e32 v48, 16, v137
	v_and_b32_e32 v49, 0xffff0000, v137
	v_pk_add_f32 v[90:91], v[90:91], v[48:49]
	v_lshlrev_b32_e32 v48, 16, v138
	v_and_b32_e32 v49, 0xffff0000, v138
	v_pk_add_f32 v[92:93], v[92:93], v[48:49]
	v_lshlrev_b32_e32 v48, 16, v139
	v_and_b32_e32 v49, 0xffff0000, v139
	v_pk_add_f32 v[94:95], v[94:95], v[48:49]
	v_lshlrev_b32_e32 v48, 16, v140
	v_and_b32_e32 v49, 0xffff0000, v140
	v_pk_add_f32 v[96:97], v[96:97], v[48:49]
	v_lshlrev_b32_e32 v48, 16, v141
	v_and_b32_e32 v49, 0xffff0000, v141
	v_pk_add_f32 v[98:99], v[98:99], v[48:49]
	v_lshlrev_b32_e32 v48, 16, v142
	v_and_b32_e32 v49, 0xffff0000, v142
	v_pk_add_f32 v[100:101], v[100:101], v[48:49]
	v_lshlrev_b32_e32 v48, 16, v143
	v_and_b32_e32 v49, 0xffff0000, v143
	v_pk_add_f32 v[102:103], v[102:103], v[48:49]
	s_cmp_lt_u32 s11, 3
	s_cbranch_scc1 .Lfin_accd0_0
	v_lshlrev_b32_e32 v48, 16, v144
	v_and_b32_e32 v49, 0xffff0000, v144
	v_pk_add_f32 v[88:89], v[88:89], v[48:49]
	v_lshlrev_b32_e32 v48, 16, v145
	v_and_b32_e32 v49, 0xffff0000, v145
	v_pk_add_f32 v[90:91], v[90:91], v[48:49]
	v_lshlrev_b32_e32 v48, 16, v146
	v_and_b32_e32 v49, 0xffff0000, v146
	v_pk_add_f32 v[92:93], v[92:93], v[48:49]
	v_lshlrev_b32_e32 v48, 16, v147
	v_and_b32_e32 v49, 0xffff0000, v147
	v_pk_add_f32 v[94:95], v[94:95], v[48:49]
	v_lshlrev_b32_e32 v48, 16, v148
	v_and_b32_e32 v49, 0xffff0000, v148
	v_pk_add_f32 v[96:97], v[96:97], v[48:49]
	v_lshlrev_b32_e32 v48, 16, v149
	v_and_b32_e32 v49, 0xffff0000, v149
	v_pk_add_f32 v[98:99], v[98:99], v[48:49]
	v_lshlrev_b32_e32 v48, 16, v150
	v_and_b32_e32 v49, 0xffff0000, v150
	v_pk_add_f32 v[100:101], v[100:101], v[48:49]
	v_lshlrev_b32_e32 v48, 16, v151
	v_and_b32_e32 v49, 0xffff0000, v151
	v_pk_add_f32 v[102:103], v[102:103], v[48:49]
	s_cmp_lt_u32 s11, 4
	s_cbranch_scc1 .Lfin_accd0_0
	v_lshlrev_b32_e32 v48, 16, v152
	v_and_b32_e32 v49, 0xffff0000, v152
	v_pk_add_f32 v[88:89], v[88:89], v[48:49]
	v_lshlrev_b32_e32 v48, 16, v153
	v_and_b32_e32 v49, 0xffff0000, v153
	v_pk_add_f32 v[90:91], v[90:91], v[48:49]
	v_lshlrev_b32_e32 v48, 16, v154
	v_and_b32_e32 v49, 0xffff0000, v154
	v_pk_add_f32 v[92:93], v[92:93], v[48:49]
	v_lshlrev_b32_e32 v48, 16, v155
	v_and_b32_e32 v49, 0xffff0000, v155
	v_pk_add_f32 v[94:95], v[94:95], v[48:49]
	v_lshlrev_b32_e32 v48, 16, v156
	v_and_b32_e32 v49, 0xffff0000, v156
	v_pk_add_f32 v[96:97], v[96:97], v[48:49]
	v_lshlrev_b32_e32 v48, 16, v157
	v_and_b32_e32 v49, 0xffff0000, v157
	v_pk_add_f32 v[98:99], v[98:99], v[48:49]
	v_lshlrev_b32_e32 v48, 16, v158
	v_and_b32_e32 v49, 0xffff0000, v158
	v_pk_add_f32 v[100:101], v[100:101], v[48:49]
	v_lshlrev_b32_e32 v48, 16, v159
	v_and_b32_e32 v49, 0xffff0000, v159
	v_pk_add_f32 v[102:103], v[102:103], v[48:49]
.Lfin_ovf0_0:
	s_cmp_eq_u32 s9, 0
	s_cbranch_scc1 .Lfin_accd0_0
	s_ff1_i32_b32 s26, s9
	s_bitset0_b32 s9, s26
	v_readlane_b32 s30, v44, s26
	s_lshl_b32 s26, s26, 11
	s_add_i32 s26, s26, s22
	s_add_i32 s26, s26, s30
	s_lshl_b32 s26, s26, 11
	s_add_u32 s24, s14, s26
	s_addc_u32 s25, s15, 0
	global_load_dwordx4 v[128:131], v1, s[24:25]
	global_load_dwordx4 v[132:135], v1, s[24:25] offset:1024
	s_waitcnt vmcnt(0)
	v_lshlrev_b32_e32 v48, 16, v128
	v_and_b32_e32 v49, 0xffff0000, v128
	v_pk_add_f32 v[88:89], v[88:89], v[48:49]
	v_lshlrev_b32_e32 v48, 16, v129
	v_and_b32_e32 v49, 0xffff0000, v129
	v_pk_add_f32 v[90:91], v[90:91], v[48:49]
	v_lshlrev_b32_e32 v48, 16, v130
	v_and_b32_e32 v49, 0xffff0000, v130
	v_pk_add_f32 v[92:93], v[92:93], v[48:49]
	v_lshlrev_b32_e32 v48, 16, v131
	v_and_b32_e32 v49, 0xffff0000, v131
	v_pk_add_f32 v[94:95], v[94:95], v[48:49]
	v_lshlrev_b32_e32 v48, 16, v132
	v_and_b32_e32 v49, 0xffff0000, v132
	v_pk_add_f32 v[96:97], v[96:97], v[48:49]
	v_lshlrev_b32_e32 v48, 16, v133
	v_and_b32_e32 v49, 0xffff0000, v133
	v_pk_add_f32 v[98:99], v[98:99], v[48:49]
	v_lshlrev_b32_e32 v48, 16, v134
	v_and_b32_e32 v49, 0xffff0000, v134
	v_pk_add_f32 v[100:101], v[100:101], v[48:49]
	v_lshlrev_b32_e32 v48, 16, v135
	v_and_b32_e32 v49, 0xffff0000, v135
	v_pk_add_f32 v[102:103], v[102:103], v[48:49]
	s_branch .Lfin_ovf0_0
.Lfin_accd0_0:
	s_add_i32 s26, s10, -1
	s_and_b32 s10, s10, s26
	s_add_i32 s26, s10, -1
	s_and_b32 s10, s10, s26
	s_add_i32 s26, s10, -1
	s_and_b32 s10, s10, s26
	s_add_i32 s26, s10, -1
	s_and_b32 s10, s10, s26
	s_cmp_lt_u32 s12, 1
	s_cbranch_scc1 .Lfin_accd0_1
	v_lshlrev_b32_e32 v48, 16, v160
	v_and_b32_e32 v49, 0xffff0000, v160
	v_pk_add_f32 v[104:105], v[104:105], v[48:49]
	v_lshlrev_b32_e32 v48, 16, v161
	v_and_b32_e32 v49, 0xffff0000, v161
	v_pk_add_f32 v[106:107], v[106:107], v[48:49]
	v_lshlrev_b32_e32 v48, 16, v162
	v_and_b32_e32 v49, 0xffff0000, v162
	v_pk_add_f32 v[108:109], v[108:109], v[48:49]
	v_lshlrev_b32_e32 v48, 16, v163
	v_and_b32_e32 v49, 0xffff0000, v163
	v_pk_add_f32 v[110:111], v[110:111], v[48:49]
	v_lshlrev_b32_e32 v48, 16, v164
	v_and_b32_e32 v49, 0xffff0000, v164
	v_pk_add_f32 v[112:113], v[112:113], v[48:49]
	v_lshlrev_b32_e32 v48, 16, v165
	v_and_b32_e32 v49, 0xffff0000, v165
	v_pk_add_f32 v[114:115], v[114:115], v[48:49]
	v_lshlrev_b32_e32 v48, 16, v166
	v_and_b32_e32 v49, 0xffff0000, v166
	v_pk_add_f32 v[116:117], v[116:117], v[48:49]
	v_lshlrev_b32_e32 v48, 16, v167
	v_and_b32_e32 v49, 0xffff0000, v167
	v_pk_add_f32 v[118:119], v[118:119], v[48:49]
	s_cmp_lt_u32 s12, 2
	s_cbranch_scc1 .Lfin_accd0_1
	v_lshlrev_b32_e32 v48, 16, v168
	v_and_b32_e32 v49, 0xffff0000, v168
	v_pk_add_f32 v[104:105], v[104:105], v[48:49]
	v_lshlrev_b32_e32 v48, 16, v169
	v_and_b32_e32 v49, 0xffff0000, v169
	v_pk_add_f32 v[106:107], v[106:107], v[48:49]
	v_lshlrev_b32_e32 v48, 16, v170
	v_and_b32_e32 v49, 0xffff0000, v170
	v_pk_add_f32 v[108:109], v[108:109], v[48:49]
	v_lshlrev_b32_e32 v48, 16, v171
	v_and_b32_e32 v49, 0xffff0000, v171
	v_pk_add_f32 v[110:111], v[110:111], v[48:49]
	v_lshlrev_b32_e32 v48, 16, v172
	v_and_b32_e32 v49, 0xffff0000, v172
	v_pk_add_f32 v[112:113], v[112:113], v[48:49]
	v_lshlrev_b32_e32 v48, 16, v173
	v_and_b32_e32 v49, 0xffff0000, v173
	v_pk_add_f32 v[114:115], v[114:115], v[48:49]
	v_lshlrev_b32_e32 v48, 16, v174
	v_and_b32_e32 v49, 0xffff0000, v174
	v_pk_add_f32 v[116:117], v[116:117], v[48:49]
	v_lshlrev_b32_e32 v48, 16, v175
	v_and_b32_e32 v49, 0xffff0000, v175
	v_pk_add_f32 v[118:119], v[118:119], v[48:49]
	s_cmp_lt_u32 s12, 3
	s_cbranch_scc1 .Lfin_accd0_1
	v_lshlrev_b32_e32 v48, 16, v176
	v_and_b32_e32 v49, 0xffff0000, v176
	v_pk_add_f32 v[104:105], v[104:105], v[48:49]
	v_lshlrev_b32_e32 v48, 16, v177
	v_and_b32_e32 v49, 0xffff0000, v177
	v_pk_add_f32 v[106:107], v[106:107], v[48:49]
	v_lshlrev_b32_e32 v48, 16, v178
	v_and_b32_e32 v49, 0xffff0000, v178
	v_pk_add_f32 v[108:109], v[108:109], v[48:49]
	v_lshlrev_b32_e32 v48, 16, v179
	v_and_b32_e32 v49, 0xffff0000, v179
	v_pk_add_f32 v[110:111], v[110:111], v[48:49]
	v_lshlrev_b32_e32 v48, 16, v180
	v_and_b32_e32 v49, 0xffff0000, v180
	v_pk_add_f32 v[112:113], v[112:113], v[48:49]
	v_lshlrev_b32_e32 v48, 16, v181
	v_and_b32_e32 v49, 0xffff0000, v181
	v_pk_add_f32 v[114:115], v[114:115], v[48:49]
	v_lshlrev_b32_e32 v48, 16, v182
	v_and_b32_e32 v49, 0xffff0000, v182
	v_pk_add_f32 v[116:117], v[116:117], v[48:49]
	v_lshlrev_b32_e32 v48, 16, v183
	v_and_b32_e32 v49, 0xffff0000, v183
	v_pk_add_f32 v[118:119], v[118:119], v[48:49]
	s_cmp_lt_u32 s12, 4
	s_cbranch_scc1 .Lfin_accd0_1
	v_lshlrev_b32_e32 v48, 16, v184
	v_and_b32_e32 v49, 0xffff0000, v184
	v_pk_add_f32 v[104:105], v[104:105], v[48:49]
	v_lshlrev_b32_e32 v48, 16, v185
	v_and_b32_e32 v49, 0xffff0000, v185
	v_pk_add_f32 v[106:107], v[106:107], v[48:49]
	v_lshlrev_b32_e32 v48, 16, v186
	v_and_b32_e32 v49, 0xffff0000, v186
	v_pk_add_f32 v[108:109], v[108:109], v[48:49]
	v_lshlrev_b32_e32 v48, 16, v187
	v_and_b32_e32 v49, 0xffff0000, v187
	v_pk_add_f32 v[110:111], v[110:111], v[48:49]
	v_lshlrev_b32_e32 v48, 16, v188
	v_and_b32_e32 v49, 0xffff0000, v188
	v_pk_add_f32 v[112:113], v[112:113], v[48:49]
	v_lshlrev_b32_e32 v48, 16, v189
	v_and_b32_e32 v49, 0xffff0000, v189
	v_pk_add_f32 v[114:115], v[114:115], v[48:49]
	v_lshlrev_b32_e32 v48, 16, v190
	v_and_b32_e32 v49, 0xffff0000, v190
	v_pk_add_f32 v[116:117], v[116:117], v[48:49]
	v_lshlrev_b32_e32 v48, 16, v191
	v_and_b32_e32 v49, 0xffff0000, v191
	v_pk_add_f32 v[118:119], v[118:119], v[48:49]
.Lfin_ovf0_1:
	s_cmp_eq_u32 s10, 0
	s_cbranch_scc1 .Lfin_accd0_1
	s_ff1_i32_b32 s26, s10
	s_bitset0_b32 s10, s26
	s_add_i32 s27, s26, 16
	v_readlane_b32 s30, v44, s27
	s_lshl_b32 s26, s26, 11
	s_add_i32 s26, s26, s22
	s_add_i32 s26, s26, s30
	s_lshl_b32 s26, s26, 11
	s_add_u32 s24, s14, s26
	s_addc_u32 s25, s15, 0
	global_load_dwordx4 v[160:163], v1, s[24:25]
	global_load_dwordx4 v[164:167], v1, s[24:25] offset:1024
	s_waitcnt vmcnt(0)
	v_lshlrev_b32_e32 v48, 16, v160
	v_and_b32_e32 v49, 0xffff0000, v160
	v_pk_add_f32 v[104:105], v[104:105], v[48:49]
	v_lshlrev_b32_e32 v48, 16, v161
	v_and_b32_e32 v49, 0xffff0000, v161
	v_pk_add_f32 v[106:107], v[106:107], v[48:49]
	v_lshlrev_b32_e32 v48, 16, v162
	v_and_b32_e32 v49, 0xffff0000, v162
	v_pk_add_f32 v[108:109], v[108:109], v[48:49]
	v_lshlrev_b32_e32 v48, 16, v163
	v_and_b32_e32 v49, 0xffff0000, v163
	v_pk_add_f32 v[110:111], v[110:111], v[48:49]
	v_lshlrev_b32_e32 v48, 16, v164
	v_and_b32_e32 v49, 0xffff0000, v164
	v_pk_add_f32 v[112:113], v[112:113], v[48:49]
	v_lshlrev_b32_e32 v48, 16, v165
	v_and_b32_e32 v49, 0xffff0000, v165
	v_pk_add_f32 v[114:115], v[114:115], v[48:49]
	v_lshlrev_b32_e32 v48, 16, v166
	v_and_b32_e32 v49, 0xffff0000, v166
	v_pk_add_f32 v[116:117], v[116:117], v[48:49]
	v_lshlrev_b32_e32 v48, 16, v167
	v_and_b32_e32 v49, 0xffff0000, v167
	v_pk_add_f32 v[118:119], v[118:119], v[48:49]
	s_branch .Lfin_ovf0_1
.Lfin_accd0_1:
	v_pk_fma_f32 v[56:57], v[88:89], v[28:29], v[56:57]
	v_pk_fma_f32 v[58:59], v[90:91], v[30:31], v[58:59]
	v_pk_fma_f32 v[60:61], v[92:93], v[32:33], v[60:61]
	v_pk_fma_f32 v[62:63], v[94:95], v[34:35], v[62:63]
	v_pk_fma_f32 v[64:65], v[96:97], v[36:37], v[64:65]
	v_pk_fma_f32 v[66:67], v[98:99], v[38:39], v[66:67]
	v_pk_fma_f32 v[68:69], v[100:101], v[40:41], v[68:69]
	v_pk_fma_f32 v[70:71], v[102:103], v[42:43], v[70:71]
	v_pk_fma_f32 v[72:73], v[104:105], v[28:29], v[72:73]
	v_pk_fma_f32 v[74:75], v[106:107], v[30:31], v[74:75]
	v_pk_fma_f32 v[76:77], v[108:109], v[32:33], v[76:77]
	v_pk_fma_f32 v[78:79], v[110:111], v[34:35], v[78:79]
	v_pk_fma_f32 v[80:81], v[112:113], v[36:37], v[80:81]
	v_pk_fma_f32 v[82:83], v[114:115], v[38:39], v[82:83]
	v_pk_fma_f32 v[84:85], v[116:117], v[40:41], v[84:85]
	v_pk_fma_f32 v[86:87], v[118:119], v[42:43], v[86:87]
	v_mul_f32_e32 v50, v56, v56
	v_mul_f32_e32 v52, v72, v72
	v_fmac_f32_e32 v50, v57, v57
	v_fmac_f32_e32 v52, v73, v73
	v_fmac_f32_e32 v50, v58, v58
	v_fmac_f32_e32 v52, v74, v74
	v_fmac_f32_e32 v50, v59, v59
	v_fmac_f32_e32 v52, v75, v75
	v_fmac_f32_e32 v50, v60, v60
	v_fmac_f32_e32 v52, v76, v76
	v_fmac_f32_e32 v50, v61, v61
	v_fmac_f32_e32 v52, v77, v77
	v_fmac_f32_e32 v50, v62, v62
	v_fmac_f32_e32 v52, v78, v78
	v_fmac_f32_e32 v50, v63, v63
	v_fmac_f32_e32 v52, v79, v79
	v_fmac_f32_e32 v50, v64, v64
	v_fmac_f32_e32 v52, v80, v80
	v_fmac_f32_e32 v50, v65, v65
	v_fmac_f32_e32 v52, v81, v81
	v_fmac_f32_e32 v50, v66, v66
	v_fmac_f32_e32 v52, v82, v82
	v_fmac_f32_e32 v50, v67, v67
	v_fmac_f32_e32 v52, v83, v83
	v_fmac_f32_e32 v50, v68, v68
	v_fmac_f32_e32 v52, v84, v84
	v_fmac_f32_e32 v50, v69, v69
	v_fmac_f32_e32 v52, v85, v85
	v_fmac_f32_e32 v50, v70, v70
	v_fmac_f32_e32 v52, v86, v86
	v_fmac_f32_e32 v50, v71, v71
	v_fmac_f32_e32 v52, v87, v87
	ds_bpermute_b32 v54, v4, v50
	ds_bpermute_b32 v55, v4, v52
	s_waitcnt lgkmcnt(1)
	v_add_f32_e32 v50, v50, v54
	s_waitcnt lgkmcnt(0)
	v_add_f32_e32 v52, v52, v55
	ds_bpermute_b32 v54, v5, v50
	ds_bpermute_b32 v55, v5, v52
	s_waitcnt lgkmcnt(1)
	v_add_f32_e32 v50, v50, v54
	s_waitcnt lgkmcnt(0)
	v_add_f32_e32 v52, v52, v55
	ds_bpermute_b32 v54, v6, v50
	ds_bpermute_b32 v55, v6, v52
	s_waitcnt lgkmcnt(1)
	v_add_f32_e32 v50, v50, v54
	s_waitcnt lgkmcnt(0)
	v_add_f32_e32 v52, v52, v55
	ds_bpermute_b32 v54, v7, v50
	ds_bpermute_b32 v55, v7, v52
	s_waitcnt lgkmcnt(1)
	v_add_f32_e32 v50, v50, v54
	s_waitcnt lgkmcnt(0)
	v_add_f32_e32 v52, v52, v55
	ds_bpermute_b32 v54, v8, v50
	ds_bpermute_b32 v55, v8, v52
	s_waitcnt lgkmcnt(1)
	v_add_f32_e32 v50, v50, v54
	s_waitcnt lgkmcnt(0)
	v_add_f32_e32 v52, v52, v55
	ds_bpermute_b32 v54, v9, v50
	ds_bpermute_b32 v55, v9, v52
	s_waitcnt lgkmcnt(1)
	v_add_f32_e32 v50, v50, v54
	s_waitcnt lgkmcnt(0)
	v_add_f32_e32 v52, v52, v55
	v_fma_f32 v50, v50, s23, v10
	v_fma_f32 v52, v52, s23, v10
	v_rsq_f32_e32 v50, v50
	v_rsq_f32_e32 v52, v52
	s_add_i32 s8, s6, 0
	s_lshl_b32 s26, s8, 12
	s_add_u32 s28, s2, s26
	s_addc_u32 s29, s3, 0
	s_add_u32 s30, s28, 0x1000
	s_addc_u32 s31, s29, 0
	v_pk_mul_f32 v[56:57], v[56:57], v[50:51] op_sel_hi:[1,0]
	v_pk_mul_f32 v[58:59], v[58:59], v[50:51] op_sel_hi:[1,0]
	v_pk_mul_f32 v[60:61], v[60:61], v[50:51] op_sel_hi:[1,0]
	v_pk_mul_f32 v[62:63], v[62:63], v[50:51] op_sel_hi:[1,0]
	v_pk_mul_f32 v[64:65], v[64:65], v[50:51] op_sel_hi:[1,0]
	v_pk_mul_f32 v[66:67], v[66:67], v[50:51] op_sel_hi:[1,0]
	v_pk_mul_f32 v[68:69], v[68:69], v[50:51] op_sel_hi:[1,0]
	v_pk_mul_f32 v[70:71], v[70:71], v[50:51] op_sel_hi:[1,0]
	v_pk_mul_f32 v[56:57], v[56:57], v[12:13]
	v_pk_mul_f32 v[58:59], v[58:59], v[14:15]
	v_pk_mul_f32 v[60:61], v[60:61], v[16:17]
	v_pk_mul_f32 v[62:63], v[62:63], v[18:19]
	v_pk_mul_f32 v[64:65], v[64:65], v[20:21]
	v_pk_mul_f32 v[66:67], v[66:67], v[22:23]
	v_pk_mul_f32 v[68:69], v[68:69], v[24:25]
	v_pk_mul_f32 v[70:71], v[70:71], v[26:27]
	global_store_dwordx4 v2, v[56:59], s[28:29]
	global_store_dwordx4 v2, v[60:63], s[28:29] offset:16
	global_store_dwordx4 v2, v[64:67], s[28:29] offset:2048
	global_store_dwordx4 v2, v[68:71], s[28:29] offset:2064
	v_pk_mul_f32 v[72:73], v[72:73], v[52:53] op_sel_hi:[1,0]
	v_pk_mul_f32 v[74:75], v[74:75], v[52:53] op_sel_hi:[1,0]
	v_pk_mul_f32 v[76:77], v[76:77], v[52:53] op_sel_hi:[1,0]
	v_pk_mul_f32 v[78:79], v[78:79], v[52:53] op_sel_hi:[1,0]
	v_pk_mul_f32 v[80:81], v[80:81], v[52:53] op_sel_hi:[1,0]
	v_pk_mul_f32 v[82:83], v[82:83], v[52:53] op_sel_hi:[1,0]
	v_pk_mul_f32 v[84:85], v[84:85], v[52:53] op_sel_hi:[1,0]
	v_pk_mul_f32 v[86:87], v[86:87], v[52:53] op_sel_hi:[1,0]
	v_pk_mul_f32 v[72:73], v[72:73], v[12:13]
	v_pk_mul_f32 v[74:75], v[74:75], v[14:15]
	v_pk_mul_f32 v[76:77], v[76:77], v[16:17]
	v_pk_mul_f32 v[78:79], v[78:79], v[18:19]
	v_pk_mul_f32 v[80:81], v[80:81], v[20:21]
	v_pk_mul_f32 v[82:83], v[82:83], v[22:23]
	v_pk_mul_f32 v[84:85], v[84:85], v[24:25]
	v_pk_mul_f32 v[86:87], v[86:87], v[26:27]
	global_store_dwordx4 v2, v[72:75], s[30:31]
	global_store_dwordx4 v2, v[76:79], s[30:31] offset:16
	global_store_dwordx4 v2, v[80:83], s[30:31] offset:2048
	global_store_dwordx4 v2, v[84:87], s[30:31] offset:2064
	v_cmp_lt_i32_e32 vcc, -1, v46
	s_mov_b32 s22, 1024
	s_and_b32 s9, vcc_lo, 0xffff
	s_lshr_b32 s10, vcc_lo, 16
	s_and_b32 s10, s10, 0xffff
	s_cmp_eq_u32 s9, 0
	s_cbranch_scc1 .Lfin_dm2_0_0
	s_ff1_i32_b32 s26, s9
	s_bitset0_b32 s9, s26
	v_readlane_b32 s30, v46, s26
	s_lshl_b32 s26, s26, 11
	s_add_i32 s26, s26, s22
	s_add_i32 s26, s26, s30
	s_lshl_b32 s26, s26, 11
	s_add_u32 s24, s14, s26
	s_addc_u32 s25, s15, 0
	s_branch .Lfin_go2_0_0

.Lfin_go2_0_0:
	global_load_dwordx4 v[128:131], v1, s[24:25]
	global_load_dwordx4 v[132:135], v1, s[24:25] offset:1024
	s_cmp_eq_u32 s9, 0
	s_cbranch_scc1 .Lfin_dm2_0_1
	s_ff1_i32_b32 s26, s9
	s_bitset0_b32 s9, s26
	v_readlane_b32 s30, v46, s26
	s_lshl_b32 s26, s26, 11
	s_add_i32 s26, s26, s22
	s_add_i32 s26, s26, s30
	s_lshl_b32 s26, s26, 11
	s_add_u32 s24, s14, s26
	s_addc_u32 s25, s15, 0
	s_branch .Lfin_go2_0_1

.Lfin_go2_0_1:
	global_load_dwordx4 v[136:139], v1, s[24:25]
	global_load_dwordx4 v[140:143], v1, s[24:25] offset:1024
	s_cmp_eq_u32 s9, 0
	s_cbranch_scc1 .Lfin_dm2_0_2
	s_ff1_i32_b32 s26, s9
	s_bitset0_b32 s9, s26
	v_readlane_b32 s30, v46, s26
	s_lshl_b32 s26, s26, 11
	s_add_i32 s26, s26, s22
	s_add_i32 s26, s26, s30
	s_lshl_b32 s26, s26, 11
	s_add_u32 s24, s14, s26
	s_addc_u32 s25, s15, 0
	s_branch .Lfin_go2_0_2

.Lfin_go2_0_2:
	global_load_dwordx4 v[144:147], v1, s[24:25]
	global_load_dwordx4 v[148:151], v1, s[24:25] offset:1024
	s_cmp_eq_u32 s9, 0
	s_cbranch_scc1 .Lfin_dm2_0_3
	s_ff1_i32_b32 s26, s9
	s_bitset0_b32 s9, s26
	v_readlane_b32 s30, v46, s26
	s_lshl_b32 s26, s26, 11
	s_add_i32 s26, s26, s22
	s_add_i32 s26, s26, s30
	s_lshl_b32 s26, s26, 11
	s_add_u32 s24, s14, s26
	s_addc_u32 s25, s15, 0
	s_branch .Lfin_go2_0_3

.Lfin_go2_0_3:
	global_load_dwordx4 v[152:155], v1, s[24:25]
	global_load_dwordx4 v[156:159], v1, s[24:25] offset:1024
	s_cmp_eq_u32 s10, 0
	s_cbranch_scc1 .Lfin_dm2_1_0
	s_ff1_i32_b32 s26, s10
	s_bitset0_b32 s10, s26
	s_add_i32 s27, s26, 16
	v_readlane_b32 s30, v46, s27
	s_lshl_b32 s26, s26, 11
	s_add_i32 s26, s26, s22
	s_add_i32 s26, s26, s30
	s_lshl_b32 s26, s26, 11
	s_add_u32 s24, s14, s26
	s_addc_u32 s25, s15, 0
	s_branch .Lfin_go2_1_0

.Lfin_go2_1_0:
	global_load_dwordx4 v[160:163], v1, s[24:25]
	global_load_dwordx4 v[164:167], v1, s[24:25] offset:1024
	s_cmp_eq_u32 s10, 0
	s_cbranch_scc1 .Lfin_dm2_1_1
	s_ff1_i32_b32 s26, s10
	s_bitset0_b32 s10, s26
	s_add_i32 s27, s26, 16
	v_readlane_b32 s30, v46, s27
	s_lshl_b32 s26, s26, 11
	s_add_i32 s26, s26, s22
	s_add_i32 s26, s26, s30
	s_lshl_b32 s26, s26, 11
	s_add_u32 s24, s14, s26
	s_addc_u32 s25, s15, 0
	s_branch .Lfin_go2_1_1

.Lfin_go2_1_1:
	global_load_dwordx4 v[168:171], v1, s[24:25]
	global_load_dwordx4 v[172:175], v1, s[24:25] offset:1024
	s_cmp_eq_u32 s10, 0
	s_cbranch_scc1 .Lfin_dm2_1_2
	s_ff1_i32_b32 s26, s10
	s_bitset0_b32 s10, s26
	s_add_i32 s27, s26, 16
	v_readlane_b32 s30, v46, s27
	s_lshl_b32 s26, s26, 11
	s_add_i32 s26, s26, s22
	s_add_i32 s26, s26, s30
	s_lshl_b32 s26, s26, 11
	s_add_u32 s24, s14, s26
	s_addc_u32 s25, s15, 0
	s_branch .Lfin_go2_1_2

.Lfin_go2_1_2:
	global_load_dwordx4 v[176:179], v1, s[24:25]
	global_load_dwordx4 v[180:183], v1, s[24:25] offset:1024
	s_cmp_eq_u32 s10, 0
	s_cbranch_scc1 .Lfin_dm2_1_3
	s_ff1_i32_b32 s26, s10
	s_bitset0_b32 s10, s26
	s_add_i32 s27, s26, 16
	v_readlane_b32 s30, v46, s27
	s_lshl_b32 s26, s26, 11
	s_add_i32 s26, s26, s22
	s_add_i32 s26, s26, s30
	s_lshl_b32 s26, s26, 11
	s_add_u32 s24, s14, s26
	s_addc_u32 s25, s15, 0
	s_branch .Lfin_go2_1_3

.Lfin_go2_1_3:
	global_load_dwordx4 v[184:187], v1, s[24:25]
	global_load_dwordx4 v[188:191], v1, s[24:25] offset:1024
	s_waitcnt vmcnt(24)
	ds_read_b128 v[88:91], v11
	ds_read_b128 v[92:95], v11 offset:1024
	ds_read_b128 v[96:99], v11 offset:2048
	ds_read_b128 v[100:103], v11 offset:3072
	v_add_u32_e32 v11, 0x1000, v11
	s_waitcnt lgkmcnt(0)
	v_cvt_f32_f16_e32 v56, v88
	v_cvt_f32_f16_sdwa v57, v88 dst_sel:DWORD dst_unused:UNUSED_PAD src0_sel:WORD_1
	v_cvt_f32_f16_e32 v58, v89
	v_cvt_f32_f16_sdwa v59, v89 dst_sel:DWORD dst_unused:UNUSED_PAD src0_sel:WORD_1
	v_cvt_f32_f16_e32 v60, v90
	v_cvt_f32_f16_sdwa v61, v90 dst_sel:DWORD dst_unused:UNUSED_PAD src0_sel:WORD_1
	v_cvt_f32_f16_e32 v62, v91
	v_cvt_f32_f16_sdwa v63, v91 dst_sel:DWORD dst_unused:UNUSED_PAD src0_sel:WORD_1
	v_cvt_f32_f16_e32 v64, v92
	v_cvt_f32_f16_sdwa v65, v92 dst_sel:DWORD dst_unused:UNUSED_PAD src0_sel:WORD_1
	v_cvt_f32_f16_e32 v66, v93
	v_cvt_f32_f16_sdwa v67, v93 dst_sel:DWORD dst_unused:UNUSED_PAD src0_sel:WORD_1
	v_cvt_f32_f16_e32 v68, v94
	v_cvt_f32_f16_sdwa v69, v94 dst_sel:DWORD dst_unused:UNUSED_PAD src0_sel:WORD_1
	v_cvt_f32_f16_e32 v70, v95
	v_cvt_f32_f16_sdwa v71, v95 dst_sel:DWORD dst_unused:UNUSED_PAD src0_sel:WORD_1
	v_cvt_f32_f16_e32 v72, v96
	v_cvt_f32_f16_sdwa v73, v96 dst_sel:DWORD dst_unused:UNUSED_PAD src0_sel:WORD_1
	v_cvt_f32_f16_e32 v74, v97
	v_cvt_f32_f16_sdwa v75, v97 dst_sel:DWORD dst_unused:UNUSED_PAD src0_sel:WORD_1
	v_cvt_f32_f16_e32 v76, v98
	v_cvt_f32_f16_sdwa v77, v98 dst_sel:DWORD dst_unused:UNUSED_PAD src0_sel:WORD_1
	v_cvt_f32_f16_e32 v78, v99
	v_cvt_f32_f16_sdwa v79, v99 dst_sel:DWORD dst_unused:UNUSED_PAD src0_sel:WORD_1
	v_cvt_f32_f16_e32 v80, v100
	v_cvt_f32_f16_sdwa v81, v100 dst_sel:DWORD dst_unused:UNUSED_PAD src0_sel:WORD_1
	v_cvt_f32_f16_e32 v82, v101
	v_cvt_f32_f16_sdwa v83, v101 dst_sel:DWORD dst_unused:UNUSED_PAD src0_sel:WORD_1
	v_cvt_f32_f16_e32 v84, v102
	v_cvt_f32_f16_sdwa v85, v102 dst_sel:DWORD dst_unused:UNUSED_PAD src0_sel:WORD_1
	v_cvt_f32_f16_e32 v86, v103
	v_cvt_f32_f16_sdwa v87, v103 dst_sel:DWORD dst_unused:UNUSED_PAD src0_sel:WORD_1
	v_cmp_lt_i32_e32 vcc, -1, v45
	s_mov_b32 s22, 0
	s_and_b32 s9, vcc_lo, 0xffff
	s_lshr_b32 s10, vcc_lo, 16
	s_and_b32 s10, s10, 0xffff
	s_bcnt1_i32_b32 s11, s9
	s_bcnt1_i32_b32 s12, s10
	v_mov_b32_e32 v88, 0
	v_mov_b32_e32 v89, 0
	v_mov_b32_e32 v90, 0
	v_mov_b32_e32 v91, 0
	v_mov_b32_e32 v92, 0
	v_mov_b32_e32 v93, 0
	v_mov_b32_e32 v94, 0
	v_mov_b32_e32 v95, 0
	v_mov_b32_e32 v96, 0
	v_mov_b32_e32 v97, 0
	v_mov_b32_e32 v98, 0
	v_mov_b32_e32 v99, 0
	v_mov_b32_e32 v100, 0
	v_mov_b32_e32 v101, 0
	v_mov_b32_e32 v102, 0
	v_mov_b32_e32 v103, 0
	v_mov_b32_e32 v104, 0
	v_mov_b32_e32 v105, 0
	v_mov_b32_e32 v106, 0
	v_mov_b32_e32 v107, 0
	v_mov_b32_e32 v108, 0
	v_mov_b32_e32 v109, 0
	v_mov_b32_e32 v110, 0
	v_mov_b32_e32 v111, 0
	v_mov_b32_e32 v112, 0
	v_mov_b32_e32 v113, 0
	v_mov_b32_e32 v114, 0
	v_mov_b32_e32 v115, 0
	v_mov_b32_e32 v116, 0
	v_mov_b32_e32 v117, 0
	v_mov_b32_e32 v118, 0
	v_mov_b32_e32 v119, 0
	s_add_i32 s26, s9, -1
	s_and_b32 s9, s9, s26
	s_add_i32 s26, s9, -1
	s_and_b32 s9, s9, s26
	s_add_i32 s26, s9, -1
	s_and_b32 s9, s9, s26
	s_add_i32 s26, s9, -1
	s_and_b32 s9, s9, s26
	s_cmp_lt_u32 s11, 1
	s_cbranch_scc1 .Lfin_accd1_0
	v_lshlrev_b32_e32 v48, 16, v192
	v_and_b32_e32 v49, 0xffff0000, v192
	v_pk_add_f32 v[88:89], v[88:89], v[48:49]
	v_lshlrev_b32_e32 v48, 16, v193
	v_and_b32_e32 v49, 0xffff0000, v193
	v_pk_add_f32 v[90:91], v[90:91], v[48:49]
	v_lshlrev_b32_e32 v48, 16, v194
	v_and_b32_e32 v49, 0xffff0000, v194
	v_pk_add_f32 v[92:93], v[92:93], v[48:49]
	v_lshlrev_b32_e32 v48, 16, v195
	v_and_b32_e32 v49, 0xffff0000, v195
	v_pk_add_f32 v[94:95], v[94:95], v[48:49]
	v_lshlrev_b32_e32 v48, 16, v196
	v_and_b32_e32 v49, 0xffff0000, v196
	v_pk_add_f32 v[96:97], v[96:97], v[48:49]
	v_lshlrev_b32_e32 v48, 16, v197
	v_and_b32_e32 v49, 0xffff0000, v197
	v_pk_add_f32 v[98:99], v[98:99], v[48:49]
	v_lshlrev_b32_e32 v48, 16, v198
	v_and_b32_e32 v49, 0xffff0000, v198
	v_pk_add_f32 v[100:101], v[100:101], v[48:49]
	v_lshlrev_b32_e32 v48, 16, v199
	v_and_b32_e32 v49, 0xffff0000, v199
	v_pk_add_f32 v[102:103], v[102:103], v[48:49]
	s_cmp_lt_u32 s11, 2
	s_cbranch_scc1 .Lfin_accd1_0
	v_lshlrev_b32_e32 v48, 16, v200
	v_and_b32_e32 v49, 0xffff0000, v200
	v_pk_add_f32 v[88:89], v[88:89], v[48:49]
	v_lshlrev_b32_e32 v48, 16, v201
	v_and_b32_e32 v49, 0xffff0000, v201
	v_pk_add_f32 v[90:91], v[90:91], v[48:49]
	v_lshlrev_b32_e32 v48, 16, v202
	v_and_b32_e32 v49, 0xffff0000, v202
	v_pk_add_f32 v[92:93], v[92:93], v[48:49]
	v_lshlrev_b32_e32 v48, 16, v203
	v_and_b32_e32 v49, 0xffff0000, v203
	v_pk_add_f32 v[94:95], v[94:95], v[48:49]
	v_lshlrev_b32_e32 v48, 16, v204
	v_and_b32_e32 v49, 0xffff0000, v204
	v_pk_add_f32 v[96:97], v[96:97], v[48:49]
	v_lshlrev_b32_e32 v48, 16, v205
	v_and_b32_e32 v49, 0xffff0000, v205
	v_pk_add_f32 v[98:99], v[98:99], v[48:49]
	v_lshlrev_b32_e32 v48, 16, v206
	v_and_b32_e32 v49, 0xffff0000, v206
	v_pk_add_f32 v[100:101], v[100:101], v[48:49]
	v_lshlrev_b32_e32 v48, 16, v207
	v_and_b32_e32 v49, 0xffff0000, v207
	v_pk_add_f32 v[102:103], v[102:103], v[48:49]
	s_cmp_lt_u32 s11, 3
	s_cbranch_scc1 .Lfin_accd1_0
	v_lshlrev_b32_e32 v48, 16, v208
	v_and_b32_e32 v49, 0xffff0000, v208
	v_pk_add_f32 v[88:89], v[88:89], v[48:49]
	v_lshlrev_b32_e32 v48, 16, v209
	v_and_b32_e32 v49, 0xffff0000, v209
	v_pk_add_f32 v[90:91], v[90:91], v[48:49]
	v_lshlrev_b32_e32 v48, 16, v210
	v_and_b32_e32 v49, 0xffff0000, v210
	v_pk_add_f32 v[92:93], v[92:93], v[48:49]
	v_lshlrev_b32_e32 v48, 16, v211
	v_and_b32_e32 v49, 0xffff0000, v211
	v_pk_add_f32 v[94:95], v[94:95], v[48:49]
	v_lshlrev_b32_e32 v48, 16, v212
	v_and_b32_e32 v49, 0xffff0000, v212
	v_pk_add_f32 v[96:97], v[96:97], v[48:49]
	v_lshlrev_b32_e32 v48, 16, v213
	v_and_b32_e32 v49, 0xffff0000, v213
	v_pk_add_f32 v[98:99], v[98:99], v[48:49]
	v_lshlrev_b32_e32 v48, 16, v214
	v_and_b32_e32 v49, 0xffff0000, v214
	v_pk_add_f32 v[100:101], v[100:101], v[48:49]
	v_lshlrev_b32_e32 v48, 16, v215
	v_and_b32_e32 v49, 0xffff0000, v215
	v_pk_add_f32 v[102:103], v[102:103], v[48:49]
	s_cmp_lt_u32 s11, 4
	s_cbranch_scc1 .Lfin_accd1_0
	v_lshlrev_b32_e32 v48, 16, v216
	v_and_b32_e32 v49, 0xffff0000, v216
	v_pk_add_f32 v[88:89], v[88:89], v[48:49]
	v_lshlrev_b32_e32 v48, 16, v217
	v_and_b32_e32 v49, 0xffff0000, v217
	v_pk_add_f32 v[90:91], v[90:91], v[48:49]
	v_lshlrev_b32_e32 v48, 16, v218
	v_and_b32_e32 v49, 0xffff0000, v218
	v_pk_add_f32 v[92:93], v[92:93], v[48:49]
	v_lshlrev_b32_e32 v48, 16, v219
	v_and_b32_e32 v49, 0xffff0000, v219
	v_pk_add_f32 v[94:95], v[94:95], v[48:49]
	v_lshlrev_b32_e32 v48, 16, v220
	v_and_b32_e32 v49, 0xffff0000, v220
	v_pk_add_f32 v[96:97], v[96:97], v[48:49]
	v_lshlrev_b32_e32 v48, 16, v221
	v_and_b32_e32 v49, 0xffff0000, v221
	v_pk_add_f32 v[98:99], v[98:99], v[48:49]
	v_lshlrev_b32_e32 v48, 16, v222
	v_and_b32_e32 v49, 0xffff0000, v222
	v_pk_add_f32 v[100:101], v[100:101], v[48:49]
	v_lshlrev_b32_e32 v48, 16, v223
	v_and_b32_e32 v49, 0xffff0000, v223
	v_pk_add_f32 v[102:103], v[102:103], v[48:49]
.Lfin_ovf1_0:
	s_cmp_eq_u32 s9, 0
	s_cbranch_scc1 .Lfin_accd1_0
	s_ff1_i32_b32 s26, s9
	s_bitset0_b32 s9, s26
	v_readlane_b32 s30, v45, s26
	s_lshl_b32 s26, s26, 11
	s_add_i32 s26, s26, s22
	s_add_i32 s26, s26, s30
	s_lshl_b32 s26, s26, 11
	s_add_u32 s24, s14, s26
	s_addc_u32 s25, s15, 0
	global_load_dwordx4 v[192:195], v1, s[24:25]
	global_load_dwordx4 v[196:199], v1, s[24:25] offset:1024
	s_waitcnt vmcnt(0)
	v_lshlrev_b32_e32 v48, 16, v192
	v_and_b32_e32 v49, 0xffff0000, v192
	v_pk_add_f32 v[88:89], v[88:89], v[48:49]
	v_lshlrev_b32_e32 v48, 16, v193
	v_and_b32_e32 v49, 0xffff0000, v193
	v_pk_add_f32 v[90:91], v[90:91], v[48:49]
	v_lshlrev_b32_e32 v48, 16, v194
	v_and_b32_e32 v49, 0xffff0000, v194
	v_pk_add_f32 v[92:93], v[92:93], v[48:49]
	v_lshlrev_b32_e32 v48, 16, v195
	v_and_b32_e32 v49, 0xffff0000, v195
	v_pk_add_f32 v[94:95], v[94:95], v[48:49]
	v_lshlrev_b32_e32 v48, 16, v196
	v_and_b32_e32 v49, 0xffff0000, v196
	v_pk_add_f32 v[96:97], v[96:97], v[48:49]
	v_lshlrev_b32_e32 v48, 16, v197
	v_and_b32_e32 v49, 0xffff0000, v197
	v_pk_add_f32 v[98:99], v[98:99], v[48:49]
	v_lshlrev_b32_e32 v48, 16, v198
	v_and_b32_e32 v49, 0xffff0000, v198
	v_pk_add_f32 v[100:101], v[100:101], v[48:49]
	v_lshlrev_b32_e32 v48, 16, v199
	v_and_b32_e32 v49, 0xffff0000, v199
	v_pk_add_f32 v[102:103], v[102:103], v[48:49]
	s_branch .Lfin_ovf1_0
.Lfin_accd1_0:
	s_add_i32 s26, s10, -1
	s_and_b32 s10, s10, s26
	s_add_i32 s26, s10, -1
	s_and_b32 s10, s10, s26
	s_add_i32 s26, s10, -1
	s_and_b32 s10, s10, s26
	s_add_i32 s26, s10, -1
	s_and_b32 s10, s10, s26
	s_cmp_lt_u32 s12, 1
	s_cbranch_scc1 .Lfin_accd1_1
	v_lshlrev_b32_e32 v48, 16, v224
	v_and_b32_e32 v49, 0xffff0000, v224
	v_pk_add_f32 v[104:105], v[104:105], v[48:49]
	v_lshlrev_b32_e32 v48, 16, v225
	v_and_b32_e32 v49, 0xffff0000, v225
	v_pk_add_f32 v[106:107], v[106:107], v[48:49]
	v_lshlrev_b32_e32 v48, 16, v226
	v_and_b32_e32 v49, 0xffff0000, v226
	v_pk_add_f32 v[108:109], v[108:109], v[48:49]
	v_lshlrev_b32_e32 v48, 16, v227
	v_and_b32_e32 v49, 0xffff0000, v227
	v_pk_add_f32 v[110:111], v[110:111], v[48:49]
	v_lshlrev_b32_e32 v48, 16, v228
	v_and_b32_e32 v49, 0xffff0000, v228
	v_pk_add_f32 v[112:113], v[112:113], v[48:49]
	v_lshlrev_b32_e32 v48, 16, v229
	v_and_b32_e32 v49, 0xffff0000, v229
	v_pk_add_f32 v[114:115], v[114:115], v[48:49]
	v_lshlrev_b32_e32 v48, 16, v230
	v_and_b32_e32 v49, 0xffff0000, v230
	v_pk_add_f32 v[116:117], v[116:117], v[48:49]
	v_lshlrev_b32_e32 v48, 16, v231
	v_and_b32_e32 v49, 0xffff0000, v231
	v_pk_add_f32 v[118:119], v[118:119], v[48:49]
	s_cmp_lt_u32 s12, 2
	s_cbranch_scc1 .Lfin_accd1_1
	v_lshlrev_b32_e32 v48, 16, v232
	v_and_b32_e32 v49, 0xffff0000, v232
	v_pk_add_f32 v[104:105], v[104:105], v[48:49]
	v_lshlrev_b32_e32 v48, 16, v233
	v_and_b32_e32 v49, 0xffff0000, v233
	v_pk_add_f32 v[106:107], v[106:107], v[48:49]
	v_lshlrev_b32_e32 v48, 16, v234
	v_and_b32_e32 v49, 0xffff0000, v234
	v_pk_add_f32 v[108:109], v[108:109], v[48:49]
	v_lshlrev_b32_e32 v48, 16, v235
	v_and_b32_e32 v49, 0xffff0000, v235
	v_pk_add_f32 v[110:111], v[110:111], v[48:49]
	v_lshlrev_b32_e32 v48, 16, v236
	v_and_b32_e32 v49, 0xffff0000, v236
	v_pk_add_f32 v[112:113], v[112:113], v[48:49]
	v_lshlrev_b32_e32 v48, 16, v237
	v_and_b32_e32 v49, 0xffff0000, v237
	v_pk_add_f32 v[114:115], v[114:115], v[48:49]
	v_lshlrev_b32_e32 v48, 16, v238
	v_and_b32_e32 v49, 0xffff0000, v238
	v_pk_add_f32 v[116:117], v[116:117], v[48:49]
	v_lshlrev_b32_e32 v48, 16, v239
	v_and_b32_e32 v49, 0xffff0000, v239
	v_pk_add_f32 v[118:119], v[118:119], v[48:49]
	s_cmp_lt_u32 s12, 3
	s_cbranch_scc1 .Lfin_accd1_1
	v_lshlrev_b32_e32 v48, 16, v240
	v_and_b32_e32 v49, 0xffff0000, v240
	v_pk_add_f32 v[104:105], v[104:105], v[48:49]
	v_lshlrev_b32_e32 v48, 16, v241
	v_and_b32_e32 v49, 0xffff0000, v241
	v_pk_add_f32 v[106:107], v[106:107], v[48:49]
	v_lshlrev_b32_e32 v48, 16, v242
	v_and_b32_e32 v49, 0xffff0000, v242
	v_pk_add_f32 v[108:109], v[108:109], v[48:49]
	v_lshlrev_b32_e32 v48, 16, v243
	v_and_b32_e32 v49, 0xffff0000, v243
	v_pk_add_f32 v[110:111], v[110:111], v[48:49]
	v_lshlrev_b32_e32 v48, 16, v244
	v_and_b32_e32 v49, 0xffff0000, v244
	v_pk_add_f32 v[112:113], v[112:113], v[48:49]
	v_lshlrev_b32_e32 v48, 16, v245
	v_and_b32_e32 v49, 0xffff0000, v245
	v_pk_add_f32 v[114:115], v[114:115], v[48:49]
	v_lshlrev_b32_e32 v48, 16, v246
	v_and_b32_e32 v49, 0xffff0000, v246
	v_pk_add_f32 v[116:117], v[116:117], v[48:49]
	v_lshlrev_b32_e32 v48, 16, v247
	v_and_b32_e32 v49, 0xffff0000, v247
	v_pk_add_f32 v[118:119], v[118:119], v[48:49]
	s_cmp_lt_u32 s12, 4
	s_cbranch_scc1 .Lfin_accd1_1
	v_lshlrev_b32_e32 v48, 16, v248
	v_and_b32_e32 v49, 0xffff0000, v248
	v_pk_add_f32 v[104:105], v[104:105], v[48:49]
	v_lshlrev_b32_e32 v48, 16, v249
	v_and_b32_e32 v49, 0xffff0000, v249
	v_pk_add_f32 v[106:107], v[106:107], v[48:49]
	v_lshlrev_b32_e32 v48, 16, v250
	v_and_b32_e32 v49, 0xffff0000, v250
	v_pk_add_f32 v[108:109], v[108:109], v[48:49]
	v_lshlrev_b32_e32 v48, 16, v251
	v_and_b32_e32 v49, 0xffff0000, v251
	v_pk_add_f32 v[110:111], v[110:111], v[48:49]
	v_lshlrev_b32_e32 v48, 16, v252
	v_and_b32_e32 v49, 0xffff0000, v252
	v_pk_add_f32 v[112:113], v[112:113], v[48:49]
	v_lshlrev_b32_e32 v48, 16, v253
	v_and_b32_e32 v49, 0xffff0000, v253
	v_pk_add_f32 v[114:115], v[114:115], v[48:49]
	v_lshlrev_b32_e32 v48, 16, v254
	v_and_b32_e32 v49, 0xffff0000, v254
	v_pk_add_f32 v[116:117], v[116:117], v[48:49]
	v_lshlrev_b32_e32 v48, 16, v255
	v_and_b32_e32 v49, 0xffff0000, v255
	v_pk_add_f32 v[118:119], v[118:119], v[48:49]
.Lfin_ovf1_1:
	s_cmp_eq_u32 s10, 0
	s_cbranch_scc1 .Lfin_accd1_1
	s_ff1_i32_b32 s26, s10
	s_bitset0_b32 s10, s26
	s_add_i32 s27, s26, 16
	v_readlane_b32 s30, v45, s27
	s_lshl_b32 s26, s26, 11
	s_add_i32 s26, s26, s22
	s_add_i32 s26, s26, s30
	s_lshl_b32 s26, s26, 11
	s_add_u32 s24, s14, s26
	s_addc_u32 s25, s15, 0
	global_load_dwordx4 v[224:227], v1, s[24:25]
	global_load_dwordx4 v[228:231], v1, s[24:25] offset:1024
	s_waitcnt vmcnt(0)
	v_lshlrev_b32_e32 v48, 16, v224
	v_and_b32_e32 v49, 0xffff0000, v224
	v_pk_add_f32 v[104:105], v[104:105], v[48:49]
	v_lshlrev_b32_e32 v48, 16, v225
	v_and_b32_e32 v49, 0xffff0000, v225
	v_pk_add_f32 v[106:107], v[106:107], v[48:49]
	v_lshlrev_b32_e32 v48, 16, v226
	v_and_b32_e32 v49, 0xffff0000, v226
	v_pk_add_f32 v[108:109], v[108:109], v[48:49]
	v_lshlrev_b32_e32 v48, 16, v227
	v_and_b32_e32 v49, 0xffff0000, v227
	v_pk_add_f32 v[110:111], v[110:111], v[48:49]
	v_lshlrev_b32_e32 v48, 16, v228
	v_and_b32_e32 v49, 0xffff0000, v228
	v_pk_add_f32 v[112:113], v[112:113], v[48:49]
	v_lshlrev_b32_e32 v48, 16, v229
	v_and_b32_e32 v49, 0xffff0000, v229
	v_pk_add_f32 v[114:115], v[114:115], v[48:49]
	v_lshlrev_b32_e32 v48, 16, v230
	v_and_b32_e32 v49, 0xffff0000, v230
	v_pk_add_f32 v[116:117], v[116:117], v[48:49]
	v_lshlrev_b32_e32 v48, 16, v231
	v_and_b32_e32 v49, 0xffff0000, v231
	v_pk_add_f32 v[118:119], v[118:119], v[48:49]
	s_branch .Lfin_ovf1_1
.Lfin_accd1_1:
	v_pk_fma_f32 v[56:57], v[88:89], v[28:29], v[56:57]
	v_pk_fma_f32 v[58:59], v[90:91], v[30:31], v[58:59]
	v_pk_fma_f32 v[60:61], v[92:93], v[32:33], v[60:61]
	v_pk_fma_f32 v[62:63], v[94:95], v[34:35], v[62:63]
	v_pk_fma_f32 v[64:65], v[96:97], v[36:37], v[64:65]
	v_pk_fma_f32 v[66:67], v[98:99], v[38:39], v[66:67]
	v_pk_fma_f32 v[68:69], v[100:101], v[40:41], v[68:69]
	v_pk_fma_f32 v[70:71], v[102:103], v[42:43], v[70:71]
	v_pk_fma_f32 v[72:73], v[104:105], v[28:29], v[72:73]
	v_pk_fma_f32 v[74:75], v[106:107], v[30:31], v[74:75]
	v_pk_fma_f32 v[76:77], v[108:109], v[32:33], v[76:77]
	v_pk_fma_f32 v[78:79], v[110:111], v[34:35], v[78:79]
	v_pk_fma_f32 v[80:81], v[112:113], v[36:37], v[80:81]
	v_pk_fma_f32 v[82:83], v[114:115], v[38:39], v[82:83]
	v_pk_fma_f32 v[84:85], v[116:117], v[40:41], v[84:85]
	v_pk_fma_f32 v[86:87], v[118:119], v[42:43], v[86:87]
	v_mul_f32_e32 v50, v56, v56
	v_mul_f32_e32 v52, v72, v72
	v_fmac_f32_e32 v50, v57, v57
	v_fmac_f32_e32 v52, v73, v73
	v_fmac_f32_e32 v50, v58, v58
	v_fmac_f32_e32 v52, v74, v74
	v_fmac_f32_e32 v50, v59, v59
	v_fmac_f32_e32 v52, v75, v75
	v_fmac_f32_e32 v50, v60, v60
	v_fmac_f32_e32 v52, v76, v76
	v_fmac_f32_e32 v50, v61, v61
	v_fmac_f32_e32 v52, v77, v77
	v_fmac_f32_e32 v50, v62, v62
	v_fmac_f32_e32 v52, v78, v78
	v_fmac_f32_e32 v50, v63, v63
	v_fmac_f32_e32 v52, v79, v79
	v_fmac_f32_e32 v50, v64, v64
	v_fmac_f32_e32 v52, v80, v80
	v_fmac_f32_e32 v50, v65, v65
	v_fmac_f32_e32 v52, v81, v81
	v_fmac_f32_e32 v50, v66, v66
	v_fmac_f32_e32 v52, v82, v82
	v_fmac_f32_e32 v50, v67, v67
	v_fmac_f32_e32 v52, v83, v83
	v_fmac_f32_e32 v50, v68, v68
	v_fmac_f32_e32 v52, v84, v84
	v_fmac_f32_e32 v50, v69, v69
	v_fmac_f32_e32 v52, v85, v85
	v_fmac_f32_e32 v50, v70, v70
	v_fmac_f32_e32 v52, v86, v86
	v_fmac_f32_e32 v50, v71, v71
	v_fmac_f32_e32 v52, v87, v87
	ds_bpermute_b32 v54, v4, v50
	ds_bpermute_b32 v55, v4, v52
	s_waitcnt lgkmcnt(1)
	v_add_f32_e32 v50, v50, v54
	s_waitcnt lgkmcnt(0)
	v_add_f32_e32 v52, v52, v55
	ds_bpermute_b32 v54, v5, v50
	ds_bpermute_b32 v55, v5, v52
	s_waitcnt lgkmcnt(1)
	v_add_f32_e32 v50, v50, v54
	s_waitcnt lgkmcnt(0)
	v_add_f32_e32 v52, v52, v55
	ds_bpermute_b32 v54, v6, v50
	ds_bpermute_b32 v55, v6, v52
	s_waitcnt lgkmcnt(1)
	v_add_f32_e32 v50, v50, v54
	s_waitcnt lgkmcnt(0)
	v_add_f32_e32 v52, v52, v55
	ds_bpermute_b32 v54, v7, v50
	ds_bpermute_b32 v55, v7, v52
	s_waitcnt lgkmcnt(1)
	v_add_f32_e32 v50, v50, v54
	s_waitcnt lgkmcnt(0)
	v_add_f32_e32 v52, v52, v55
	ds_bpermute_b32 v54, v8, v50
	ds_bpermute_b32 v55, v8, v52
	s_waitcnt lgkmcnt(1)
	v_add_f32_e32 v50, v50, v54
	s_waitcnt lgkmcnt(0)
	v_add_f32_e32 v52, v52, v55
	ds_bpermute_b32 v54, v9, v50
	ds_bpermute_b32 v55, v9, v52
	s_waitcnt lgkmcnt(1)
	v_add_f32_e32 v50, v50, v54
	s_waitcnt lgkmcnt(0)
	v_add_f32_e32 v52, v52, v55
	v_fma_f32 v50, v50, s23, v10
	v_fma_f32 v52, v52, s23, v10
	v_rsq_f32_e32 v50, v50
	v_rsq_f32_e32 v52, v52
	s_add_i32 s8, s6, 4096
	s_lshl_b32 s26, s8, 12
	s_add_u32 s28, s2, s26
	s_addc_u32 s29, s3, 0
	s_add_u32 s30, s28, 0x1000
	s_addc_u32 s31, s29, 0
	v_pk_mul_f32 v[56:57], v[56:57], v[50:51] op_sel_hi:[1,0]
	v_pk_mul_f32 v[58:59], v[58:59], v[50:51] op_sel_hi:[1,0]
	v_pk_mul_f32 v[60:61], v[60:61], v[50:51] op_sel_hi:[1,0]
	v_pk_mul_f32 v[62:63], v[62:63], v[50:51] op_sel_hi:[1,0]
	v_pk_mul_f32 v[64:65], v[64:65], v[50:51] op_sel_hi:[1,0]
	v_pk_mul_f32 v[66:67], v[66:67], v[50:51] op_sel_hi:[1,0]
	v_pk_mul_f32 v[68:69], v[68:69], v[50:51] op_sel_hi:[1,0]
	v_pk_mul_f32 v[70:71], v[70:71], v[50:51] op_sel_hi:[1,0]
	v_pk_mul_f32 v[56:57], v[56:57], v[12:13]
	v_pk_mul_f32 v[58:59], v[58:59], v[14:15]
	v_pk_mul_f32 v[60:61], v[60:61], v[16:17]
	v_pk_mul_f32 v[62:63], v[62:63], v[18:19]
	v_pk_mul_f32 v[64:65], v[64:65], v[20:21]
	v_pk_mul_f32 v[66:67], v[66:67], v[22:23]
	v_pk_mul_f32 v[68:69], v[68:69], v[24:25]
	v_pk_mul_f32 v[70:71], v[70:71], v[26:27]
	global_store_dwordx4 v2, v[56:59], s[28:29]
	global_store_dwordx4 v2, v[60:63], s[28:29] offset:16
	global_store_dwordx4 v2, v[64:67], s[28:29] offset:2048
	global_store_dwordx4 v2, v[68:71], s[28:29] offset:2064
	v_pk_mul_f32 v[72:73], v[72:73], v[52:53] op_sel_hi:[1,0]
	v_pk_mul_f32 v[74:75], v[74:75], v[52:53] op_sel_hi:[1,0]
	v_pk_mul_f32 v[76:77], v[76:77], v[52:53] op_sel_hi:[1,0]
	v_pk_mul_f32 v[78:79], v[78:79], v[52:53] op_sel_hi:[1,0]
	v_pk_mul_f32 v[80:81], v[80:81], v[52:53] op_sel_hi:[1,0]
	v_pk_mul_f32 v[82:83], v[82:83], v[52:53] op_sel_hi:[1,0]
	v_pk_mul_f32 v[84:85], v[84:85], v[52:53] op_sel_hi:[1,0]
	v_pk_mul_f32 v[86:87], v[86:87], v[52:53] op_sel_hi:[1,0]
	v_pk_mul_f32 v[72:73], v[72:73], v[12:13]
	v_pk_mul_f32 v[74:75], v[74:75], v[14:15]
	v_pk_mul_f32 v[76:77], v[76:77], v[16:17]
	v_pk_mul_f32 v[78:79], v[78:79], v[18:19]
	v_pk_mul_f32 v[80:81], v[80:81], v[20:21]
	v_pk_mul_f32 v[82:83], v[82:83], v[22:23]
	v_pk_mul_f32 v[84:85], v[84:85], v[24:25]
	v_pk_mul_f32 v[86:87], v[86:87], v[26:27]
	global_store_dwordx4 v2, v[72:75], s[30:31]
	global_store_dwordx4 v2, v[76:79], s[30:31] offset:16
	global_store_dwordx4 v2, v[80:83], s[30:31] offset:2048
	global_store_dwordx4 v2, v[84:87], s[30:31] offset:2064
	global_load_dwordx4 v[28:31], v2, s[34:35]
	global_load_dwordx4 v[32:35], v2, s[34:35] offset:16
	global_load_dwordx4 v[36:39], v2, s[34:35] offset:2048
	global_load_dwordx4 v[40:43], v2, s[34:35] offset:2064
	v_cmp_lt_i32_e32 vcc, -1, v47
	s_mov_b32 s22, 1024
	s_and_b32 s9, vcc_lo, 0xffff
	s_lshr_b32 s10, vcc_lo, 16
	s_and_b32 s10, s10, 0xffff
	s_cmp_eq_u32 s9, 0
	s_cbranch_scc1 .Lfin_dm3_0_0
	s_ff1_i32_b32 s26, s9
	s_bitset0_b32 s9, s26
	v_readlane_b32 s30, v47, s26
	s_lshl_b32 s26, s26, 11
	s_add_i32 s26, s26, s22
	s_add_i32 s26, s26, s30
	s_lshl_b32 s26, s26, 11
	s_add_u32 s24, s14, s26
	s_addc_u32 s25, s15, 0
	s_branch .Lfin_go3_0_0

.Lfin_go3_0_0:
	global_load_dwordx4 v[192:195], v1, s[24:25]
	global_load_dwordx4 v[196:199], v1, s[24:25] offset:1024
	s_cmp_eq_u32 s9, 0
	s_cbranch_scc1 .Lfin_dm3_0_1
	s_ff1_i32_b32 s26, s9
	s_bitset0_b32 s9, s26
	v_readlane_b32 s30, v47, s26
	s_lshl_b32 s26, s26, 11
	s_add_i32 s26, s26, s22
	s_add_i32 s26, s26, s30
	s_lshl_b32 s26, s26, 11
	s_add_u32 s24, s14, s26
	s_addc_u32 s25, s15, 0
	s_branch .Lfin_go3_0_1

.Lfin_go3_0_1:
	global_load_dwordx4 v[200:203], v1, s[24:25]
	global_load_dwordx4 v[204:207], v1, s[24:25] offset:1024
	s_cmp_eq_u32 s9, 0
	s_cbranch_scc1 .Lfin_dm3_0_2
	s_ff1_i32_b32 s26, s9
	s_bitset0_b32 s9, s26
	v_readlane_b32 s30, v47, s26
	s_lshl_b32 s26, s26, 11
	s_add_i32 s26, s26, s22
	s_add_i32 s26, s26, s30
	s_lshl_b32 s26, s26, 11
	s_add_u32 s24, s14, s26
	s_addc_u32 s25, s15, 0
	s_branch .Lfin_go3_0_2

.Lfin_go3_0_2:
	global_load_dwordx4 v[208:211], v1, s[24:25]
	global_load_dwordx4 v[212:215], v1, s[24:25] offset:1024
	s_cmp_eq_u32 s9, 0
	s_cbranch_scc1 .Lfin_dm3_0_3
	s_ff1_i32_b32 s26, s9
	s_bitset0_b32 s9, s26
	v_readlane_b32 s30, v47, s26
	s_lshl_b32 s26, s26, 11
	s_add_i32 s26, s26, s22
	s_add_i32 s26, s26, s30
	s_lshl_b32 s26, s26, 11
	s_add_u32 s24, s14, s26
	s_addc_u32 s25, s15, 0
	s_branch .Lfin_go3_0_3

.Lfin_go3_0_3:
	global_load_dwordx4 v[216:219], v1, s[24:25]
	global_load_dwordx4 v[220:223], v1, s[24:25] offset:1024
	s_cmp_eq_u32 s10, 0
	s_cbranch_scc1 .Lfin_dm3_1_0
	s_ff1_i32_b32 s26, s10
	s_bitset0_b32 s10, s26
	s_add_i32 s27, s26, 16
	v_readlane_b32 s30, v47, s27
	s_lshl_b32 s26, s26, 11
	s_add_i32 s26, s26, s22
	s_add_i32 s26, s26, s30
	s_lshl_b32 s26, s26, 11
	s_add_u32 s24, s14, s26
	s_addc_u32 s25, s15, 0
	s_branch .Lfin_go3_1_0

.Lfin_go3_1_0:
	global_load_dwordx4 v[224:227], v1, s[24:25]
	global_load_dwordx4 v[228:231], v1, s[24:25] offset:1024
	s_cmp_eq_u32 s10, 0
	s_cbranch_scc1 .Lfin_dm3_1_1
	s_ff1_i32_b32 s26, s10
	s_bitset0_b32 s10, s26
	s_add_i32 s27, s26, 16
	v_readlane_b32 s30, v47, s27
	s_lshl_b32 s26, s26, 11
	s_add_i32 s26, s26, s22
	s_add_i32 s26, s26, s30
	s_lshl_b32 s26, s26, 11
	s_add_u32 s24, s14, s26
	s_addc_u32 s25, s15, 0
	s_branch .Lfin_go3_1_1

.Lfin_go3_1_1:
	global_load_dwordx4 v[232:235], v1, s[24:25]
	global_load_dwordx4 v[236:239], v1, s[24:25] offset:1024
	s_cmp_eq_u32 s10, 0
	s_cbranch_scc1 .Lfin_dm3_1_2
	s_ff1_i32_b32 s26, s10
	s_bitset0_b32 s10, s26
	s_add_i32 s27, s26, 16
	v_readlane_b32 s30, v47, s27
	s_lshl_b32 s26, s26, 11
	s_add_i32 s26, s26, s22
	s_add_i32 s26, s26, s30
	s_lshl_b32 s26, s26, 11
	s_add_u32 s24, s14, s26
	s_addc_u32 s25, s15, 0
	s_branch .Lfin_go3_1_2

.Lfin_go3_1_2:
	global_load_dwordx4 v[240:243], v1, s[24:25]
	global_load_dwordx4 v[244:247], v1, s[24:25] offset:1024
	s_cmp_eq_u32 s10, 0
	s_cbranch_scc1 .Lfin_dm3_1_3
	s_ff1_i32_b32 s26, s10
	s_bitset0_b32 s10, s26
	s_add_i32 s27, s26, 16
	v_readlane_b32 s30, v47, s27
	s_lshl_b32 s26, s26, 11
	s_add_i32 s26, s26, s22
	s_add_i32 s26, s26, s30
	s_lshl_b32 s26, s26, 11
	s_add_u32 s24, s14, s26
	s_addc_u32 s25, s15, 0
	s_branch .Lfin_go3_1_3

.Lfin_go3_1_3:
	global_load_dwordx4 v[248:251], v1, s[24:25]
	global_load_dwordx4 v[252:255], v1, s[24:25] offset:1024
	s_waitcnt vmcnt(28)
	ds_read_b128 v[88:91], v11
	ds_read_b128 v[92:95], v11 offset:1024
	ds_read_b128 v[96:99], v11 offset:2048
	ds_read_b128 v[100:103], v11 offset:3072
	v_add_u32_e32 v11, 0x1000, v11
	s_waitcnt lgkmcnt(0)
	v_cvt_f32_f16_e32 v56, v88
	v_cvt_f32_f16_sdwa v57, v88 dst_sel:DWORD dst_unused:UNUSED_PAD src0_sel:WORD_1
	v_cvt_f32_f16_e32 v58, v89
	v_cvt_f32_f16_sdwa v59, v89 dst_sel:DWORD dst_unused:UNUSED_PAD src0_sel:WORD_1
	v_cvt_f32_f16_e32 v60, v90
	v_cvt_f32_f16_sdwa v61, v90 dst_sel:DWORD dst_unused:UNUSED_PAD src0_sel:WORD_1
	v_cvt_f32_f16_e32 v62, v91
	v_cvt_f32_f16_sdwa v63, v91 dst_sel:DWORD dst_unused:UNUSED_PAD src0_sel:WORD_1
	v_cvt_f32_f16_e32 v64, v92
	v_cvt_f32_f16_sdwa v65, v92 dst_sel:DWORD dst_unused:UNUSED_PAD src0_sel:WORD_1
	v_cvt_f32_f16_e32 v66, v93
	v_cvt_f32_f16_sdwa v67, v93 dst_sel:DWORD dst_unused:UNUSED_PAD src0_sel:WORD_1
	v_cvt_f32_f16_e32 v68, v94
	v_cvt_f32_f16_sdwa v69, v94 dst_sel:DWORD dst_unused:UNUSED_PAD src0_sel:WORD_1
	v_cvt_f32_f16_e32 v70, v95
	v_cvt_f32_f16_sdwa v71, v95 dst_sel:DWORD dst_unused:UNUSED_PAD src0_sel:WORD_1
	v_cvt_f32_f16_e32 v72, v96
	v_cvt_f32_f16_sdwa v73, v96 dst_sel:DWORD dst_unused:UNUSED_PAD src0_sel:WORD_1
	v_cvt_f32_f16_e32 v74, v97
	v_cvt_f32_f16_sdwa v75, v97 dst_sel:DWORD dst_unused:UNUSED_PAD src0_sel:WORD_1
	v_cvt_f32_f16_e32 v76, v98
	v_cvt_f32_f16_sdwa v77, v98 dst_sel:DWORD dst_unused:UNUSED_PAD src0_sel:WORD_1
	v_cvt_f32_f16_e32 v78, v99
	v_cvt_f32_f16_sdwa v79, v99 dst_sel:DWORD dst_unused:UNUSED_PAD src0_sel:WORD_1
	v_cvt_f32_f16_e32 v80, v100
	v_cvt_f32_f16_sdwa v81, v100 dst_sel:DWORD dst_unused:UNUSED_PAD src0_sel:WORD_1
	v_cvt_f32_f16_e32 v82, v101
	v_cvt_f32_f16_sdwa v83, v101 dst_sel:DWORD dst_unused:UNUSED_PAD src0_sel:WORD_1
	v_cvt_f32_f16_e32 v84, v102
	v_cvt_f32_f16_sdwa v85, v102 dst_sel:DWORD dst_unused:UNUSED_PAD src0_sel:WORD_1
	v_cvt_f32_f16_e32 v86, v103
	v_cvt_f32_f16_sdwa v87, v103 dst_sel:DWORD dst_unused:UNUSED_PAD src0_sel:WORD_1
	v_cmp_lt_i32_e32 vcc, -1, v46
	s_mov_b32 s22, 1024
	s_and_b32 s9, vcc_lo, 0xffff
	s_lshr_b32 s10, vcc_lo, 16
	s_and_b32 s10, s10, 0xffff
	s_bcnt1_i32_b32 s11, s9
	s_bcnt1_i32_b32 s12, s10
	v_mov_b32_e32 v88, 0
	v_mov_b32_e32 v89, 0
	v_mov_b32_e32 v90, 0
	v_mov_b32_e32 v91, 0
	v_mov_b32_e32 v92, 0
	v_mov_b32_e32 v93, 0
	v_mov_b32_e32 v94, 0
	v_mov_b32_e32 v95, 0
	v_mov_b32_e32 v96, 0
	v_mov_b32_e32 v97, 0
	v_mov_b32_e32 v98, 0
	v_mov_b32_e32 v99, 0
	v_mov_b32_e32 v100, 0
	v_mov_b32_e32 v101, 0
	v_mov_b32_e32 v102, 0
	v_mov_b32_e32 v103, 0
	v_mov_b32_e32 v104, 0
	v_mov_b32_e32 v105, 0
	v_mov_b32_e32 v106, 0
	v_mov_b32_e32 v107, 0
	v_mov_b32_e32 v108, 0
	v_mov_b32_e32 v109, 0
	v_mov_b32_e32 v110, 0
	v_mov_b32_e32 v111, 0
	v_mov_b32_e32 v112, 0
	v_mov_b32_e32 v113, 0
	v_mov_b32_e32 v114, 0
	v_mov_b32_e32 v115, 0
	v_mov_b32_e32 v116, 0
	v_mov_b32_e32 v117, 0
	v_mov_b32_e32 v118, 0
	v_mov_b32_e32 v119, 0
	s_add_i32 s26, s9, -1
	s_and_b32 s9, s9, s26
	s_add_i32 s26, s9, -1
	s_and_b32 s9, s9, s26
	s_add_i32 s26, s9, -1
	s_and_b32 s9, s9, s26
	s_add_i32 s26, s9, -1
	s_and_b32 s9, s9, s26
	s_cmp_lt_u32 s11, 1
	s_cbranch_scc1 .Lfin_accd2_0
	v_lshlrev_b32_e32 v48, 16, v128
	v_and_b32_e32 v49, 0xffff0000, v128
	v_pk_add_f32 v[88:89], v[88:89], v[48:49]
	v_lshlrev_b32_e32 v48, 16, v129
	v_and_b32_e32 v49, 0xffff0000, v129
	v_pk_add_f32 v[90:91], v[90:91], v[48:49]
	v_lshlrev_b32_e32 v48, 16, v130
	v_and_b32_e32 v49, 0xffff0000, v130
	v_pk_add_f32 v[92:93], v[92:93], v[48:49]
	v_lshlrev_b32_e32 v48, 16, v131
	v_and_b32_e32 v49, 0xffff0000, v131
	v_pk_add_f32 v[94:95], v[94:95], v[48:49]
	v_lshlrev_b32_e32 v48, 16, v132
	v_and_b32_e32 v49, 0xffff0000, v132
	v_pk_add_f32 v[96:97], v[96:97], v[48:49]
	v_lshlrev_b32_e32 v48, 16, v133
	v_and_b32_e32 v49, 0xffff0000, v133
	v_pk_add_f32 v[98:99], v[98:99], v[48:49]
	v_lshlrev_b32_e32 v48, 16, v134
	v_and_b32_e32 v49, 0xffff0000, v134
	v_pk_add_f32 v[100:101], v[100:101], v[48:49]
	v_lshlrev_b32_e32 v48, 16, v135
	v_and_b32_e32 v49, 0xffff0000, v135
	v_pk_add_f32 v[102:103], v[102:103], v[48:49]
	s_cmp_lt_u32 s11, 2
	s_cbranch_scc1 .Lfin_accd2_0
	v_lshlrev_b32_e32 v48, 16, v136
	v_and_b32_e32 v49, 0xffff0000, v136
	v_pk_add_f32 v[88:89], v[88:89], v[48:49]
	v_lshlrev_b32_e32 v48, 16, v137
	v_and_b32_e32 v49, 0xffff0000, v137
	v_pk_add_f32 v[90:91], v[90:91], v[48:49]
	v_lshlrev_b32_e32 v48, 16, v138
	v_and_b32_e32 v49, 0xffff0000, v138
	v_pk_add_f32 v[92:93], v[92:93], v[48:49]
	v_lshlrev_b32_e32 v48, 16, v139
	v_and_b32_e32 v49, 0xffff0000, v139
	v_pk_add_f32 v[94:95], v[94:95], v[48:49]
	v_lshlrev_b32_e32 v48, 16, v140
	v_and_b32_e32 v49, 0xffff0000, v140
	v_pk_add_f32 v[96:97], v[96:97], v[48:49]
	v_lshlrev_b32_e32 v48, 16, v141
	v_and_b32_e32 v49, 0xffff0000, v141
	v_pk_add_f32 v[98:99], v[98:99], v[48:49]
	v_lshlrev_b32_e32 v48, 16, v142
	v_and_b32_e32 v49, 0xffff0000, v142
	v_pk_add_f32 v[100:101], v[100:101], v[48:49]
	v_lshlrev_b32_e32 v48, 16, v143
	v_and_b32_e32 v49, 0xffff0000, v143
	v_pk_add_f32 v[102:103], v[102:103], v[48:49]
	s_cmp_lt_u32 s11, 3
	s_cbranch_scc1 .Lfin_accd2_0
	v_lshlrev_b32_e32 v48, 16, v144
	v_and_b32_e32 v49, 0xffff0000, v144
	v_pk_add_f32 v[88:89], v[88:89], v[48:49]
	v_lshlrev_b32_e32 v48, 16, v145
	v_and_b32_e32 v49, 0xffff0000, v145
	v_pk_add_f32 v[90:91], v[90:91], v[48:49]
	v_lshlrev_b32_e32 v48, 16, v146
	v_and_b32_e32 v49, 0xffff0000, v146
	v_pk_add_f32 v[92:93], v[92:93], v[48:49]
	v_lshlrev_b32_e32 v48, 16, v147
	v_and_b32_e32 v49, 0xffff0000, v147
	v_pk_add_f32 v[94:95], v[94:95], v[48:49]
	v_lshlrev_b32_e32 v48, 16, v148
	v_and_b32_e32 v49, 0xffff0000, v148
	v_pk_add_f32 v[96:97], v[96:97], v[48:49]
	v_lshlrev_b32_e32 v48, 16, v149
	v_and_b32_e32 v49, 0xffff0000, v149
	v_pk_add_f32 v[98:99], v[98:99], v[48:49]
	v_lshlrev_b32_e32 v48, 16, v150
	v_and_b32_e32 v49, 0xffff0000, v150
	v_pk_add_f32 v[100:101], v[100:101], v[48:49]
	v_lshlrev_b32_e32 v48, 16, v151
	v_and_b32_e32 v49, 0xffff0000, v151
	v_pk_add_f32 v[102:103], v[102:103], v[48:49]
	s_cmp_lt_u32 s11, 4
	s_cbranch_scc1 .Lfin_accd2_0
	v_lshlrev_b32_e32 v48, 16, v152
	v_and_b32_e32 v49, 0xffff0000, v152
	v_pk_add_f32 v[88:89], v[88:89], v[48:49]
	v_lshlrev_b32_e32 v48, 16, v153
	v_and_b32_e32 v49, 0xffff0000, v153
	v_pk_add_f32 v[90:91], v[90:91], v[48:49]
	v_lshlrev_b32_e32 v48, 16, v154
	v_and_b32_e32 v49, 0xffff0000, v154
	v_pk_add_f32 v[92:93], v[92:93], v[48:49]
	v_lshlrev_b32_e32 v48, 16, v155
	v_and_b32_e32 v49, 0xffff0000, v155
	v_pk_add_f32 v[94:95], v[94:95], v[48:49]
	v_lshlrev_b32_e32 v48, 16, v156
	v_and_b32_e32 v49, 0xffff0000, v156
	v_pk_add_f32 v[96:97], v[96:97], v[48:49]
	v_lshlrev_b32_e32 v48, 16, v157
	v_and_b32_e32 v49, 0xffff0000, v157
	v_pk_add_f32 v[98:99], v[98:99], v[48:49]
	v_lshlrev_b32_e32 v48, 16, v158
	v_and_b32_e32 v49, 0xffff0000, v158
	v_pk_add_f32 v[100:101], v[100:101], v[48:49]
	v_lshlrev_b32_e32 v48, 16, v159
	v_and_b32_e32 v49, 0xffff0000, v159
	v_pk_add_f32 v[102:103], v[102:103], v[48:49]
.Lfin_ovf2_0:
	s_cmp_eq_u32 s9, 0
	s_cbranch_scc1 .Lfin_accd2_0
	s_ff1_i32_b32 s26, s9
	s_bitset0_b32 s9, s26
	v_readlane_b32 s30, v46, s26
	s_lshl_b32 s26, s26, 11
	s_add_i32 s26, s26, s22
	s_add_i32 s26, s26, s30
	s_lshl_b32 s26, s26, 11
	s_add_u32 s24, s14, s26
	s_addc_u32 s25, s15, 0
	global_load_dwordx4 v[128:131], v1, s[24:25]
	global_load_dwordx4 v[132:135], v1, s[24:25] offset:1024
	s_waitcnt vmcnt(0)
	v_lshlrev_b32_e32 v48, 16, v128
	v_and_b32_e32 v49, 0xffff0000, v128
	v_pk_add_f32 v[88:89], v[88:89], v[48:49]
	v_lshlrev_b32_e32 v48, 16, v129
	v_and_b32_e32 v49, 0xffff0000, v129
	v_pk_add_f32 v[90:91], v[90:91], v[48:49]
	v_lshlrev_b32_e32 v48, 16, v130
	v_and_b32_e32 v49, 0xffff0000, v130
	v_pk_add_f32 v[92:93], v[92:93], v[48:49]
	v_lshlrev_b32_e32 v48, 16, v131
	v_and_b32_e32 v49, 0xffff0000, v131
	v_pk_add_f32 v[94:95], v[94:95], v[48:49]
	v_lshlrev_b32_e32 v48, 16, v132
	v_and_b32_e32 v49, 0xffff0000, v132
	v_pk_add_f32 v[96:97], v[96:97], v[48:49]
	v_lshlrev_b32_e32 v48, 16, v133
	v_and_b32_e32 v49, 0xffff0000, v133
	v_pk_add_f32 v[98:99], v[98:99], v[48:49]
	v_lshlrev_b32_e32 v48, 16, v134
	v_and_b32_e32 v49, 0xffff0000, v134
	v_pk_add_f32 v[100:101], v[100:101], v[48:49]
	v_lshlrev_b32_e32 v48, 16, v135
	v_and_b32_e32 v49, 0xffff0000, v135
	v_pk_add_f32 v[102:103], v[102:103], v[48:49]
	s_branch .Lfin_ovf2_0

.Lfin_ovf2_1:
	s_cmp_eq_u32 s10, 0
	s_cbranch_scc1 .Lfin_accd2_1
	s_ff1_i32_b32 s26, s10
	s_bitset0_b32 s10, s26
	s_add_i32 s27, s26, 16
	v_readlane_b32 s30, v46, s27
	s_lshl_b32 s26, s26, 11
	s_add_i32 s26, s26, s22
	s_add_i32 s26, s26, s30
	s_lshl_b32 s26, s26, 11
	s_add_u32 s24, s14, s26
	s_addc_u32 s25, s15, 0
	global_load_dwordx4 v[160:163], v1, s[24:25]
	global_load_dwordx4 v[164:167], v1, s[24:25] offset:1024
	s_waitcnt vmcnt(0)
	v_lshlrev_b32_e32 v48, 16, v160
	v_and_b32_e32 v49, 0xffff0000, v160
	v_pk_add_f32 v[104:105], v[104:105], v[48:49]
	v_lshlrev_b32_e32 v48, 16, v161
	v_and_b32_e32 v49, 0xffff0000, v161
	v_pk_add_f32 v[106:107], v[106:107], v[48:49]
	v_lshlrev_b32_e32 v48, 16, v162
	v_and_b32_e32 v49, 0xffff0000, v162
	v_pk_add_f32 v[108:109], v[108:109], v[48:49]
	v_lshlrev_b32_e32 v48, 16, v163
	v_and_b32_e32 v49, 0xffff0000, v163
	v_pk_add_f32 v[110:111], v[110:111], v[48:49]
	v_lshlrev_b32_e32 v48, 16, v164
	v_and_b32_e32 v49, 0xffff0000, v164
	v_pk_add_f32 v[112:113], v[112:113], v[48:49]
	v_lshlrev_b32_e32 v48, 16, v165
	v_and_b32_e32 v49, 0xffff0000, v165
	v_pk_add_f32 v[114:115], v[114:115], v[48:49]
	v_lshlrev_b32_e32 v48, 16, v166
	v_and_b32_e32 v49, 0xffff0000, v166
	v_pk_add_f32 v[116:117], v[116:117], v[48:49]
	v_lshlrev_b32_e32 v48, 16, v167
	v_and_b32_e32 v49, 0xffff0000, v167
	v_pk_add_f32 v[118:119], v[118:119], v[48:49]
	s_branch .Lfin_ovf2_1
.Lfin_accd2_1:
	s_waitcnt vmcnt(16)
	v_pk_fma_f32 v[56:57], v[88:89], v[28:29], v[56:57]
	v_pk_fma_f32 v[58:59], v[90:91], v[30:31], v[58:59]
	v_pk_fma_f32 v[60:61], v[92:93], v[32:33], v[60:61]
	v_pk_fma_f32 v[62:63], v[94:95], v[34:35], v[62:63]
	v_pk_fma_f32 v[64:65], v[96:97], v[36:37], v[64:65]
	v_pk_fma_f32 v[66:67], v[98:99], v[38:39], v[66:67]
	v_pk_fma_f32 v[68:69], v[100:101], v[40:41], v[68:69]
	v_pk_fma_f32 v[70:71], v[102:103], v[42:43], v[70:71]
	v_pk_fma_f32 v[72:73], v[104:105], v[28:29], v[72:73]
	v_pk_fma_f32 v[74:75], v[106:107], v[30:31], v[74:75]
	v_pk_fma_f32 v[76:77], v[108:109], v[32:33], v[76:77]
	v_pk_fma_f32 v[78:79], v[110:111], v[34:35], v[78:79]
	v_pk_fma_f32 v[80:81], v[112:113], v[36:37], v[80:81]
	v_pk_fma_f32 v[82:83], v[114:115], v[38:39], v[82:83]
	v_pk_fma_f32 v[84:85], v[116:117], v[40:41], v[84:85]
	v_pk_fma_f32 v[86:87], v[118:119], v[42:43], v[86:87]
	v_mul_f32_e32 v50, v56, v56
	v_mul_f32_e32 v52, v72, v72
	v_fmac_f32_e32 v50, v57, v57
	v_fmac_f32_e32 v52, v73, v73
	v_fmac_f32_e32 v50, v58, v58
	v_fmac_f32_e32 v52, v74, v74
	v_fmac_f32_e32 v50, v59, v59
	v_fmac_f32_e32 v52, v75, v75
	v_fmac_f32_e32 v50, v60, v60
	v_fmac_f32_e32 v52, v76, v76
	v_fmac_f32_e32 v50, v61, v61
	v_fmac_f32_e32 v52, v77, v77
	v_fmac_f32_e32 v50, v62, v62
	v_fmac_f32_e32 v52, v78, v78
	v_fmac_f32_e32 v50, v63, v63
	v_fmac_f32_e32 v52, v79, v79
	v_fmac_f32_e32 v50, v64, v64
	v_fmac_f32_e32 v52, v80, v80
	v_fmac_f32_e32 v50, v65, v65
	v_fmac_f32_e32 v52, v81, v81
	v_fmac_f32_e32 v50, v66, v66
	v_fmac_f32_e32 v52, v82, v82
	v_fmac_f32_e32 v50, v67, v67
	v_fmac_f32_e32 v52, v83, v83
	v_fmac_f32_e32 v50, v68, v68
	v_fmac_f32_e32 v52, v84, v84
	v_fmac_f32_e32 v50, v69, v69
	v_fmac_f32_e32 v52, v85, v85
	v_fmac_f32_e32 v50, v70, v70
	v_fmac_f32_e32 v52, v86, v86
	v_fmac_f32_e32 v50, v71, v71
	v_fmac_f32_e32 v52, v87, v87
	ds_bpermute_b32 v54, v4, v50
	ds_bpermute_b32 v55, v4, v52
	s_waitcnt lgkmcnt(1)
	v_add_f32_e32 v50, v50, v54
	s_waitcnt lgkmcnt(0)
	v_add_f32_e32 v52, v52, v55
	ds_bpermute_b32 v54, v5, v50
	ds_bpermute_b32 v55, v5, v52
	s_waitcnt lgkmcnt(1)
	v_add_f32_e32 v50, v50, v54
	s_waitcnt lgkmcnt(0)
	v_add_f32_e32 v52, v52, v55
	ds_bpermute_b32 v54, v6, v50
	ds_bpermute_b32 v55, v6, v52
	s_waitcnt lgkmcnt(1)
	v_add_f32_e32 v50, v50, v54
	s_waitcnt lgkmcnt(0)
	v_add_f32_e32 v52, v52, v55
	ds_bpermute_b32 v54, v7, v50
	ds_bpermute_b32 v55, v7, v52
	s_waitcnt lgkmcnt(1)
	v_add_f32_e32 v50, v50, v54
	s_waitcnt lgkmcnt(0)
	v_add_f32_e32 v52, v52, v55
	ds_bpermute_b32 v54, v8, v50
	ds_bpermute_b32 v55, v8, v52
	s_waitcnt lgkmcnt(1)
	v_add_f32_e32 v50, v50, v54
	s_waitcnt lgkmcnt(0)
	v_add_f32_e32 v52, v52, v55
	ds_bpermute_b32 v54, v9, v50
	ds_bpermute_b32 v55, v9, v52
	s_waitcnt lgkmcnt(1)
	v_add_f32_e32 v50, v50, v54
	s_waitcnt lgkmcnt(0)
	v_add_f32_e32 v52, v52, v55
	v_fma_f32 v50, v50, s23, v10
	v_fma_f32 v52, v52, s23, v10
	v_rsq_f32_e32 v50, v50
	v_rsq_f32_e32 v52, v52
	s_add_i32 s8, s6, 8192
	s_lshl_b32 s26, s8, 12
	s_add_u32 s28, s2, s26
	s_addc_u32 s29, s3, 0
	s_add_u32 s30, s28, 0x1000
	s_addc_u32 s31, s29, 0
	v_pk_mul_f32 v[56:57], v[56:57], v[50:51] op_sel_hi:[1,0]
	v_pk_mul_f32 v[58:59], v[58:59], v[50:51] op_sel_hi:[1,0]
	v_pk_mul_f32 v[60:61], v[60:61], v[50:51] op_sel_hi:[1,0]
	v_pk_mul_f32 v[62:63], v[62:63], v[50:51] op_sel_hi:[1,0]
	v_pk_mul_f32 v[64:65], v[64:65], v[50:51] op_sel_hi:[1,0]
	v_pk_mul_f32 v[66:67], v[66:67], v[50:51] op_sel_hi:[1,0]
	v_pk_mul_f32 v[68:69], v[68:69], v[50:51] op_sel_hi:[1,0]
	v_pk_mul_f32 v[70:71], v[70:71], v[50:51] op_sel_hi:[1,0]
	v_pk_mul_f32 v[56:57], v[56:57], v[12:13]
	v_pk_mul_f32 v[58:59], v[58:59], v[14:15]
	v_pk_mul_f32 v[60:61], v[60:61], v[16:17]
	v_pk_mul_f32 v[62:63], v[62:63], v[18:19]
	v_pk_mul_f32 v[64:65], v[64:65], v[20:21]
	v_pk_mul_f32 v[66:67], v[66:67], v[22:23]
	v_pk_mul_f32 v[68:69], v[68:69], v[24:25]
	v_pk_mul_f32 v[70:71], v[70:71], v[26:27]
	global_store_dwordx4 v2, v[56:59], s[28:29]
	global_store_dwordx4 v2, v[60:63], s[28:29] offset:16
	global_store_dwordx4 v2, v[64:67], s[28:29] offset:2048
	global_store_dwordx4 v2, v[68:71], s[28:29] offset:2064
	v_pk_mul_f32 v[72:73], v[72:73], v[52:53] op_sel_hi:[1,0]
	v_pk_mul_f32 v[74:75], v[74:75], v[52:53] op_sel_hi:[1,0]
	v_pk_mul_f32 v[76:77], v[76:77], v[52:53] op_sel_hi:[1,0]
	v_pk_mul_f32 v[78:79], v[78:79], v[52:53] op_sel_hi:[1,0]
	v_pk_mul_f32 v[80:81], v[80:81], v[52:53] op_sel_hi:[1,0]
	v_pk_mul_f32 v[82:83], v[82:83], v[52:53] op_sel_hi:[1,0]
	v_pk_mul_f32 v[84:85], v[84:85], v[52:53] op_sel_hi:[1,0]
	v_pk_mul_f32 v[86:87], v[86:87], v[52:53] op_sel_hi:[1,0]
	v_pk_mul_f32 v[72:73], v[72:73], v[12:13]
	v_pk_mul_f32 v[74:75], v[74:75], v[14:15]
	v_pk_mul_f32 v[76:77], v[76:77], v[16:17]
	v_pk_mul_f32 v[78:79], v[78:79], v[18:19]
	v_pk_mul_f32 v[80:81], v[80:81], v[20:21]
	v_pk_mul_f32 v[82:83], v[82:83], v[22:23]
	v_pk_mul_f32 v[84:85], v[84:85], v[24:25]
	v_pk_mul_f32 v[86:87], v[86:87], v[26:27]
	global_store_dwordx4 v2, v[72:75], s[30:31]
	global_store_dwordx4 v2, v[76:79], s[30:31] offset:16
	global_store_dwordx4 v2, v[80:83], s[30:31] offset:2048
	global_store_dwordx4 v2, v[84:87], s[30:31] offset:2064
	s_waitcnt vmcnt(8)
	ds_read_b128 v[88:91], v11
	ds_read_b128 v[92:95], v11 offset:1024
	ds_read_b128 v[96:99], v11 offset:2048
	ds_read_b128 v[100:103], v11 offset:3072
	v_add_u32_e32 v11, 0x1000, v11
	s_waitcnt lgkmcnt(0)
	v_cvt_f32_f16_e32 v56, v88
	v_cvt_f32_f16_sdwa v57, v88 dst_sel:DWORD dst_unused:UNUSED_PAD src0_sel:WORD_1
	v_cvt_f32_f16_e32 v58, v89
	v_cvt_f32_f16_sdwa v59, v89 dst_sel:DWORD dst_unused:UNUSED_PAD src0_sel:WORD_1
	v_cvt_f32_f16_e32 v60, v90
	v_cvt_f32_f16_sdwa v61, v90 dst_sel:DWORD dst_unused:UNUSED_PAD src0_sel:WORD_1
	v_cvt_f32_f16_e32 v62, v91
	v_cvt_f32_f16_sdwa v63, v91 dst_sel:DWORD dst_unused:UNUSED_PAD src0_sel:WORD_1
	v_cvt_f32_f16_e32 v64, v92
	v_cvt_f32_f16_sdwa v65, v92 dst_sel:DWORD dst_unused:UNUSED_PAD src0_sel:WORD_1
	v_cvt_f32_f16_e32 v66, v93
	v_cvt_f32_f16_sdwa v67, v93 dst_sel:DWORD dst_unused:UNUSED_PAD src0_sel:WORD_1
	v_cvt_f32_f16_e32 v68, v94
	v_cvt_f32_f16_sdwa v69, v94 dst_sel:DWORD dst_unused:UNUSED_PAD src0_sel:WORD_1
	v_cvt_f32_f16_e32 v70, v95
	v_cvt_f32_f16_sdwa v71, v95 dst_sel:DWORD dst_unused:UNUSED_PAD src0_sel:WORD_1
	v_cvt_f32_f16_e32 v72, v96
	v_cvt_f32_f16_sdwa v73, v96 dst_sel:DWORD dst_unused:UNUSED_PAD src0_sel:WORD_1
	v_cvt_f32_f16_e32 v74, v97
	v_cvt_f32_f16_sdwa v75, v97 dst_sel:DWORD dst_unused:UNUSED_PAD src0_sel:WORD_1
	v_cvt_f32_f16_e32 v76, v98
	v_cvt_f32_f16_sdwa v77, v98 dst_sel:DWORD dst_unused:UNUSED_PAD src0_sel:WORD_1
	v_cvt_f32_f16_e32 v78, v99
	v_cvt_f32_f16_sdwa v79, v99 dst_sel:DWORD dst_unused:UNUSED_PAD src0_sel:WORD_1
	v_cvt_f32_f16_e32 v80, v100
	v_cvt_f32_f16_sdwa v81, v100 dst_sel:DWORD dst_unused:UNUSED_PAD src0_sel:WORD_1
	v_cvt_f32_f16_e32 v82, v101
	v_cvt_f32_f16_sdwa v83, v101 dst_sel:DWORD dst_unused:UNUSED_PAD src0_sel:WORD_1
	v_cvt_f32_f16_e32 v84, v102
	v_cvt_f32_f16_sdwa v85, v102 dst_sel:DWORD dst_unused:UNUSED_PAD src0_sel:WORD_1
	v_cvt_f32_f16_e32 v86, v103
	v_cvt_f32_f16_sdwa v87, v103 dst_sel:DWORD dst_unused:UNUSED_PAD src0_sel:WORD_1
	v_cmp_lt_i32_e32 vcc, -1, v47
	s_mov_b32 s22, 1024
	s_and_b32 s9, vcc_lo, 0xffff
	s_lshr_b32 s10, vcc_lo, 16
	s_and_b32 s10, s10, 0xffff
	s_bcnt1_i32_b32 s11, s9
	s_bcnt1_i32_b32 s12, s10
	v_mov_b32_e32 v88, 0
	v_mov_b32_e32 v89, 0
	v_mov_b32_e32 v90, 0
	v_mov_b32_e32 v91, 0
	v_mov_b32_e32 v92, 0
	v_mov_b32_e32 v93, 0
	v_mov_b32_e32 v94, 0
	v_mov_b32_e32 v95, 0
	v_mov_b32_e32 v96, 0
	v_mov_b32_e32 v97, 0
	v_mov_b32_e32 v98, 0
	v_mov_b32_e32 v99, 0
	v_mov_b32_e32 v100, 0
	v_mov_b32_e32 v101, 0
	v_mov_b32_e32 v102, 0
	v_mov_b32_e32 v103, 0
	v_mov_b32_e32 v104, 0
	v_mov_b32_e32 v105, 0
	v_mov_b32_e32 v106, 0
	v_mov_b32_e32 v107, 0
	v_mov_b32_e32 v108, 0
	v_mov_b32_e32 v109, 0
	v_mov_b32_e32 v110, 0
	v_mov_b32_e32 v111, 0
	v_mov_b32_e32 v112, 0
	v_mov_b32_e32 v113, 0
	v_mov_b32_e32 v114, 0
	v_mov_b32_e32 v115, 0
	v_mov_b32_e32 v116, 0
	v_mov_b32_e32 v117, 0
	v_mov_b32_e32 v118, 0
	v_mov_b32_e32 v119, 0
	s_add_i32 s26, s9, -1
	s_and_b32 s9, s9, s26
	s_add_i32 s26, s9, -1
	s_and_b32 s9, s9, s26
	s_add_i32 s26, s9, -1
	s_and_b32 s9, s9, s26
	s_add_i32 s26, s9, -1
	s_and_b32 s9, s9, s26
	s_cmp_lt_u32 s11, 1
	s_cbranch_scc1 .Lfin_accd3_0
	v_lshlrev_b32_e32 v48, 16, v192
	v_and_b32_e32 v49, 0xffff0000, v192
	v_pk_add_f32 v[88:89], v[88:89], v[48:49]
	v_lshlrev_b32_e32 v48, 16, v193
	v_and_b32_e32 v49, 0xffff0000, v193
	v_pk_add_f32 v[90:91], v[90:91], v[48:49]
	v_lshlrev_b32_e32 v48, 16, v194
	v_and_b32_e32 v49, 0xffff0000, v194
	v_pk_add_f32 v[92:93], v[92:93], v[48:49]
	v_lshlrev_b32_e32 v48, 16, v195
	v_and_b32_e32 v49, 0xffff0000, v195
	v_pk_add_f32 v[94:95], v[94:95], v[48:49]
	v_lshlrev_b32_e32 v48, 16, v196
	v_and_b32_e32 v49, 0xffff0000, v196
	v_pk_add_f32 v[96:97], v[96:97], v[48:49]
	v_lshlrev_b32_e32 v48, 16, v197
	v_and_b32_e32 v49, 0xffff0000, v197
	v_pk_add_f32 v[98:99], v[98:99], v[48:49]
	v_lshlrev_b32_e32 v48, 16, v198
	v_and_b32_e32 v49, 0xffff0000, v198
	v_pk_add_f32 v[100:101], v[100:101], v[48:49]
	v_lshlrev_b32_e32 v48, 16, v199
	v_and_b32_e32 v49, 0xffff0000, v199
	v_pk_add_f32 v[102:103], v[102:103], v[48:49]
	s_cmp_lt_u32 s11, 2
	s_cbranch_scc1 .Lfin_accd3_0
	v_lshlrev_b32_e32 v48, 16, v200
	v_and_b32_e32 v49, 0xffff0000, v200
	v_pk_add_f32 v[88:89], v[88:89], v[48:49]
	v_lshlrev_b32_e32 v48, 16, v201
	v_and_b32_e32 v49, 0xffff0000, v201
	v_pk_add_f32 v[90:91], v[90:91], v[48:49]
	v_lshlrev_b32_e32 v48, 16, v202
	v_and_b32_e32 v49, 0xffff0000, v202
	v_pk_add_f32 v[92:93], v[92:93], v[48:49]
	v_lshlrev_b32_e32 v48, 16, v203
	v_and_b32_e32 v49, 0xffff0000, v203
	v_pk_add_f32 v[94:95], v[94:95], v[48:49]
	v_lshlrev_b32_e32 v48, 16, v204
	v_and_b32_e32 v49, 0xffff0000, v204
	v_pk_add_f32 v[96:97], v[96:97], v[48:49]
	v_lshlrev_b32_e32 v48, 16, v205
	v_and_b32_e32 v49, 0xffff0000, v205
	v_pk_add_f32 v[98:99], v[98:99], v[48:49]
	v_lshlrev_b32_e32 v48, 16, v206
	v_and_b32_e32 v49, 0xffff0000, v206
	v_pk_add_f32 v[100:101], v[100:101], v[48:49]
	v_lshlrev_b32_e32 v48, 16, v207
	v_and_b32_e32 v49, 0xffff0000, v207
	v_pk_add_f32 v[102:103], v[102:103], v[48:49]
	s_cmp_lt_u32 s11, 3
	s_cbranch_scc1 .Lfin_accd3_0
	v_lshlrev_b32_e32 v48, 16, v208
	v_and_b32_e32 v49, 0xffff0000, v208
	v_pk_add_f32 v[88:89], v[88:89], v[48:49]
	v_lshlrev_b32_e32 v48, 16, v209
	v_and_b32_e32 v49, 0xffff0000, v209
	v_pk_add_f32 v[90:91], v[90:91], v[48:49]
	v_lshlrev_b32_e32 v48, 16, v210
	v_and_b32_e32 v49, 0xffff0000, v210
	v_pk_add_f32 v[92:93], v[92:93], v[48:49]
	v_lshlrev_b32_e32 v48, 16, v211
	v_and_b32_e32 v49, 0xffff0000, v211
	v_pk_add_f32 v[94:95], v[94:95], v[48:49]
	v_lshlrev_b32_e32 v48, 16, v212
	v_and_b32_e32 v49, 0xffff0000, v212
	v_pk_add_f32 v[96:97], v[96:97], v[48:49]
	v_lshlrev_b32_e32 v48, 16, v213
	v_and_b32_e32 v49, 0xffff0000, v213
	v_pk_add_f32 v[98:99], v[98:99], v[48:49]
	v_lshlrev_b32_e32 v48, 16, v214
	v_and_b32_e32 v49, 0xffff0000, v214
	v_pk_add_f32 v[100:101], v[100:101], v[48:49]
	v_lshlrev_b32_e32 v48, 16, v215
	v_and_b32_e32 v49, 0xffff0000, v215
	v_pk_add_f32 v[102:103], v[102:103], v[48:49]
	s_cmp_lt_u32 s11, 4
	s_cbranch_scc1 .Lfin_accd3_0
	v_lshlrev_b32_e32 v48, 16, v216
	v_and_b32_e32 v49, 0xffff0000, v216
	v_pk_add_f32 v[88:89], v[88:89], v[48:49]
	v_lshlrev_b32_e32 v48, 16, v217
	v_and_b32_e32 v49, 0xffff0000, v217
	v_pk_add_f32 v[90:91], v[90:91], v[48:49]
	v_lshlrev_b32_e32 v48, 16, v218
	v_and_b32_e32 v49, 0xffff0000, v218
	v_pk_add_f32 v[92:93], v[92:93], v[48:49]
	v_lshlrev_b32_e32 v48, 16, v219
	v_and_b32_e32 v49, 0xffff0000, v219
	v_pk_add_f32 v[94:95], v[94:95], v[48:49]
	v_lshlrev_b32_e32 v48, 16, v220
	v_and_b32_e32 v49, 0xffff0000, v220
	v_pk_add_f32 v[96:97], v[96:97], v[48:49]
	v_lshlrev_b32_e32 v48, 16, v221
	v_and_b32_e32 v49, 0xffff0000, v221
	v_pk_add_f32 v[98:99], v[98:99], v[48:49]
	v_lshlrev_b32_e32 v48, 16, v222
	v_and_b32_e32 v49, 0xffff0000, v222
	v_pk_add_f32 v[100:101], v[100:101], v[48:49]
	v_lshlrev_b32_e32 v48, 16, v223
	v_and_b32_e32 v49, 0xffff0000, v223
	v_pk_add_f32 v[102:103], v[102:103], v[48:49]
.Lfin_ovf3_0:
	s_cmp_eq_u32 s9, 0
	s_cbranch_scc1 .Lfin_accd3_0
	s_ff1_i32_b32 s26, s9
	s_bitset0_b32 s9, s26
	v_readlane_b32 s30, v47, s26
	s_lshl_b32 s26, s26, 11
	s_add_i32 s26, s26, s22
	s_add_i32 s26, s26, s30
	s_lshl_b32 s26, s26, 11
	s_add_u32 s24, s14, s26
	s_addc_u32 s25, s15, 0
	global_load_dwordx4 v[192:195], v1, s[24:25]
	global_load_dwordx4 v[196:199], v1, s[24:25] offset:1024
	s_waitcnt vmcnt(0)
	v_lshlrev_b32_e32 v48, 16, v192
	v_and_b32_e32 v49, 0xffff0000, v192
	v_pk_add_f32 v[88:89], v[88:89], v[48:49]
	v_lshlrev_b32_e32 v48, 16, v193
	v_and_b32_e32 v49, 0xffff0000, v193
	v_pk_add_f32 v[90:91], v[90:91], v[48:49]
	v_lshlrev_b32_e32 v48, 16, v194
	v_and_b32_e32 v49, 0xffff0000, v194
	v_pk_add_f32 v[92:93], v[92:93], v[48:49]
	v_lshlrev_b32_e32 v48, 16, v195
	v_and_b32_e32 v49, 0xffff0000, v195
	v_pk_add_f32 v[94:95], v[94:95], v[48:49]
	v_lshlrev_b32_e32 v48, 16, v196
	v_and_b32_e32 v49, 0xffff0000, v196
	v_pk_add_f32 v[96:97], v[96:97], v[48:49]
	v_lshlrev_b32_e32 v48, 16, v197
	v_and_b32_e32 v49, 0xffff0000, v197
	v_pk_add_f32 v[98:99], v[98:99], v[48:49]
	v_lshlrev_b32_e32 v48, 16, v198
	v_and_b32_e32 v49, 0xffff0000, v198
	v_pk_add_f32 v[100:101], v[100:101], v[48:49]
	v_lshlrev_b32_e32 v48, 16, v199
	v_and_b32_e32 v49, 0xffff0000, v199
	v_pk_add_f32 v[102:103], v[102:103], v[48:49]
	s_branch .Lfin_ovf3_0

.Lfin_ovf3_1:
	s_cmp_eq_u32 s10, 0
	s_cbranch_scc1 .Lfin_accd3_1
	s_ff1_i32_b32 s26, s10
	s_bitset0_b32 s10, s26
	s_add_i32 s27, s26, 16
	v_readlane_b32 s30, v47, s27
	s_lshl_b32 s26, s26, 11
	s_add_i32 s26, s26, s22
	s_add_i32 s26, s26, s30
	s_lshl_b32 s26, s26, 11
	s_add_u32 s24, s14, s26
	s_addc_u32 s25, s15, 0
	global_load_dwordx4 v[224:227], v1, s[24:25]
	global_load_dwordx4 v[228:231], v1, s[24:25] offset:1024
	s_waitcnt vmcnt(0)
	v_lshlrev_b32_e32 v48, 16, v224
	v_and_b32_e32 v49, 0xffff0000, v224
	v_pk_add_f32 v[104:105], v[104:105], v[48:49]
	v_lshlrev_b32_e32 v48, 16, v225
	v_and_b32_e32 v49, 0xffff0000, v225
	v_pk_add_f32 v[106:107], v[106:107], v[48:49]
	v_lshlrev_b32_e32 v48, 16, v226
	v_and_b32_e32 v49, 0xffff0000, v226
	v_pk_add_f32 v[108:109], v[108:109], v[48:49]
	v_lshlrev_b32_e32 v48, 16, v227
	v_and_b32_e32 v49, 0xffff0000, v227
	v_pk_add_f32 v[110:111], v[110:111], v[48:49]
	v_lshlrev_b32_e32 v48, 16, v228
	v_and_b32_e32 v49, 0xffff0000, v228
	v_pk_add_f32 v[112:113], v[112:113], v[48:49]
	v_lshlrev_b32_e32 v48, 16, v229
	v_and_b32_e32 v49, 0xffff0000, v229
	v_pk_add_f32 v[114:115], v[114:115], v[48:49]
	v_lshlrev_b32_e32 v48, 16, v230
	v_and_b32_e32 v49, 0xffff0000, v230
	v_pk_add_f32 v[116:117], v[116:117], v[48:49]
	v_lshlrev_b32_e32 v48, 16, v231
	v_and_b32_e32 v49, 0xffff0000, v231
	v_pk_add_f32 v[118:119], v[118:119], v[48:49]
	s_branch .Lfin_ovf3_1
.Lfin_accd3_1:
	v_pk_fma_f32 v[56:57], v[88:89], v[28:29], v[56:57]
	v_pk_fma_f32 v[58:59], v[90:91], v[30:31], v[58:59]
	v_pk_fma_f32 v[60:61], v[92:93], v[32:33], v[60:61]
	v_pk_fma_f32 v[62:63], v[94:95], v[34:35], v[62:63]
	v_pk_fma_f32 v[64:65], v[96:97], v[36:37], v[64:65]
	v_pk_fma_f32 v[66:67], v[98:99], v[38:39], v[66:67]
	v_pk_fma_f32 v[68:69], v[100:101], v[40:41], v[68:69]
	v_pk_fma_f32 v[70:71], v[102:103], v[42:43], v[70:71]
	v_pk_fma_f32 v[72:73], v[104:105], v[28:29], v[72:73]
	v_pk_fma_f32 v[74:75], v[106:107], v[30:31], v[74:75]
	v_pk_fma_f32 v[76:77], v[108:109], v[32:33], v[76:77]
	v_pk_fma_f32 v[78:79], v[110:111], v[34:35], v[78:79]
	v_pk_fma_f32 v[80:81], v[112:113], v[36:37], v[80:81]
	v_pk_fma_f32 v[82:83], v[114:115], v[38:39], v[82:83]
	v_pk_fma_f32 v[84:85], v[116:117], v[40:41], v[84:85]
	v_pk_fma_f32 v[86:87], v[118:119], v[42:43], v[86:87]
	v_mul_f32_e32 v50, v56, v56
	v_mul_f32_e32 v52, v72, v72
	v_fmac_f32_e32 v50, v57, v57
	v_fmac_f32_e32 v52, v73, v73
	v_fmac_f32_e32 v50, v58, v58
	v_fmac_f32_e32 v52, v74, v74
	v_fmac_f32_e32 v50, v59, v59
	v_fmac_f32_e32 v52, v75, v75
	v_fmac_f32_e32 v50, v60, v60
	v_fmac_f32_e32 v52, v76, v76
	v_fmac_f32_e32 v50, v61, v61
	v_fmac_f32_e32 v52, v77, v77
	v_fmac_f32_e32 v50, v62, v62
	v_fmac_f32_e32 v52, v78, v78
	v_fmac_f32_e32 v50, v63, v63
	v_fmac_f32_e32 v52, v79, v79
	v_fmac_f32_e32 v50, v64, v64
	v_fmac_f32_e32 v52, v80, v80
	v_fmac_f32_e32 v50, v65, v65
	v_fmac_f32_e32 v52, v81, v81
	v_fmac_f32_e32 v50, v66, v66
	v_fmac_f32_e32 v52, v82, v82
	v_fmac_f32_e32 v50, v67, v67
	v_fmac_f32_e32 v52, v83, v83
	v_fmac_f32_e32 v50, v68, v68
	v_fmac_f32_e32 v52, v84, v84
	v_fmac_f32_e32 v50, v69, v69
	v_fmac_f32_e32 v52, v85, v85
	v_fmac_f32_e32 v50, v70, v70
	v_fmac_f32_e32 v52, v86, v86
	v_fmac_f32_e32 v50, v71, v71
	v_fmac_f32_e32 v52, v87, v87
	ds_bpermute_b32 v54, v4, v50
	ds_bpermute_b32 v55, v4, v52
	s_waitcnt lgkmcnt(1)
	v_add_f32_e32 v50, v50, v54
	s_waitcnt lgkmcnt(0)
	v_add_f32_e32 v52, v52, v55
	ds_bpermute_b32 v54, v5, v50
	ds_bpermute_b32 v55, v5, v52
	s_waitcnt lgkmcnt(1)
	v_add_f32_e32 v50, v50, v54
	s_waitcnt lgkmcnt(0)
	v_add_f32_e32 v52, v52, v55
	ds_bpermute_b32 v54, v6, v50
	ds_bpermute_b32 v55, v6, v52
	s_waitcnt lgkmcnt(1)
	v_add_f32_e32 v50, v50, v54
	s_waitcnt lgkmcnt(0)
	v_add_f32_e32 v52, v52, v55
	ds_bpermute_b32 v54, v7, v50
	ds_bpermute_b32 v55, v7, v52
	s_waitcnt lgkmcnt(1)
	v_add_f32_e32 v50, v50, v54
	s_waitcnt lgkmcnt(0)
	v_add_f32_e32 v52, v52, v55
	ds_bpermute_b32 v54, v8, v50
	ds_bpermute_b32 v55, v8, v52
	s_waitcnt lgkmcnt(1)
	v_add_f32_e32 v50, v50, v54
	s_waitcnt lgkmcnt(0)
	v_add_f32_e32 v52, v52, v55
	ds_bpermute_b32 v54, v9, v50
	ds_bpermute_b32 v55, v9, v52
	s_waitcnt lgkmcnt(1)
	v_add_f32_e32 v50, v50, v54
	s_waitcnt lgkmcnt(0)
	v_add_f32_e32 v52, v52, v55
	v_fma_f32 v50, v50, s23, v10
	v_fma_f32 v52, v52, s23, v10
	v_rsq_f32_e32 v50, v50
	v_rsq_f32_e32 v52, v52
	s_add_i32 s8, s6, 12288
	s_lshl_b32 s26, s8, 12
	s_add_u32 s28, s2, s26
	s_addc_u32 s29, s3, 0
	s_add_u32 s30, s28, 0x1000
	s_addc_u32 s31, s29, 0
	v_pk_mul_f32 v[56:57], v[56:57], v[50:51] op_sel_hi:[1,0]
	v_pk_mul_f32 v[58:59], v[58:59], v[50:51] op_sel_hi:[1,0]
	v_pk_mul_f32 v[60:61], v[60:61], v[50:51] op_sel_hi:[1,0]
	v_pk_mul_f32 v[62:63], v[62:63], v[50:51] op_sel_hi:[1,0]
	v_pk_mul_f32 v[64:65], v[64:65], v[50:51] op_sel_hi:[1,0]
	v_pk_mul_f32 v[66:67], v[66:67], v[50:51] op_sel_hi:[1,0]
	v_pk_mul_f32 v[68:69], v[68:69], v[50:51] op_sel_hi:[1,0]
	v_pk_mul_f32 v[70:71], v[70:71], v[50:51] op_sel_hi:[1,0]
	v_pk_mul_f32 v[56:57], v[56:57], v[12:13]
	v_pk_mul_f32 v[58:59], v[58:59], v[14:15]
	v_pk_mul_f32 v[60:61], v[60:61], v[16:17]
	v_pk_mul_f32 v[62:63], v[62:63], v[18:19]
	v_pk_mul_f32 v[64:65], v[64:65], v[20:21]
	v_pk_mul_f32 v[66:67], v[66:67], v[22:23]
	v_pk_mul_f32 v[68:69], v[68:69], v[24:25]
	v_pk_mul_f32 v[70:71], v[70:71], v[26:27]
	global_store_dwordx4 v2, v[56:59], s[28:29]
	global_store_dwordx4 v2, v[60:63], s[28:29] offset:16
	global_store_dwordx4 v2, v[64:67], s[28:29] offset:2048
	global_store_dwordx4 v2, v[68:71], s[28:29] offset:2064
	v_pk_mul_f32 v[72:73], v[72:73], v[52:53] op_sel_hi:[1,0]
	v_pk_mul_f32 v[74:75], v[74:75], v[52:53] op_sel_hi:[1,0]
	v_pk_mul_f32 v[76:77], v[76:77], v[52:53] op_sel_hi:[1,0]
	v_pk_mul_f32 v[78:79], v[78:79], v[52:53] op_sel_hi:[1,0]
	v_pk_mul_f32 v[80:81], v[80:81], v[52:53] op_sel_hi:[1,0]
	v_pk_mul_f32 v[82:83], v[82:83], v[52:53] op_sel_hi:[1,0]
	v_pk_mul_f32 v[84:85], v[84:85], v[52:53] op_sel_hi:[1,0]
	v_pk_mul_f32 v[86:87], v[86:87], v[52:53] op_sel_hi:[1,0]
	v_pk_mul_f32 v[72:73], v[72:73], v[12:13]
	v_pk_mul_f32 v[74:75], v[74:75], v[14:15]
	v_pk_mul_f32 v[76:77], v[76:77], v[16:17]
	v_pk_mul_f32 v[78:79], v[78:79], v[18:19]
	v_pk_mul_f32 v[80:81], v[80:81], v[20:21]
	v_pk_mul_f32 v[82:83], v[82:83], v[22:23]
	v_pk_mul_f32 v[84:85], v[84:85], v[24:25]
	v_pk_mul_f32 v[86:87], v[86:87], v[26:27]
	global_store_dwordx4 v2, v[72:75], s[30:31]
	global_store_dwordx4 v2, v[76:79], s[30:31] offset:16
	global_store_dwordx4 v2, v[80:83], s[30:31] offset:2048
	global_store_dwordx4 v2, v[84:87], s[30:31] offset:2064
	s_endpgm
